# v58 + dead rsqrt denormal fix-ups removed in 4 GEMM epilogues + attention unit drain V-fragment reads issued 4 MFMAs ahead
# baseline (speedup 1.0000x reference)
.LBB0_274:
	s_add_u32 s100, s53, 0x40080
	s_addc_u32 s101, s27, 0
	v_lshl_add_u64 v[144:145], s[100:101], 0, v[140:141]
	s_add_i32 m0, s60, 0xc000
	s_nop 0
	global_load_lds_dwordx4 v[144:145], off
	v_lshl_add_u64 v[144:145], s[100:101], 0, v[142:143]
	s_add_i32 m0, s60, 0xe000
	s_nop 0
	global_load_lds_dwordx4 v[144:145], off
	s_cmp_lt_i32 s8, 4
	v_lshl_or_b32 v144, s8, 8, v161
	s_cselect_b64 vcc, -1, 0
	s_lshl_b32 s8, s9, 12
	s_and_b32 s8, s8, 0x1000
	v_add_u32_e32 v165, s8, v160
	ds_read_b128 v[166:169], v165
	v_mov_b32_e32 v145, 0x3e38aa3b
	v_cndmask_b32_e32 v163, 1.0, v145, vcc
	v_ashrrev_i32_e32 v145, 31, v144
	v_lshl_add_u32 v164, s52, 8, v157
	s_waitcnt lgkmcnt(0)
	v_mov_b32_e32 v172, v167
	v_mov_b32_e32 v173, v168
	v_mov_b32_e32 v167, v169
	v_pk_add_f32 v[166:167], v[172:173], v[166:167]
	v_lshl_add_u64 v[144:145], v[144:145], 1, s[74:75]
	v_add_f32_e32 v166, v166, v167
	v_fmamk_f32 v166, v166, 0x3a800000, v198
	s_movk_i32 s27, 0x1800
	v_rsq_f32_e32 v166, v166
	v_mad_i64_i32 v[170:171], s[52:53], v164, s27, v[144:145]
	s_mov_b64 s[52:53], -1
	v_mul_f32_e32 v166, v163, v166
	v_pk_mul_f32 v[126:127], v[126:127], v[166:167] op_sel_hi:[1,0]
	v_pk_mul_f32 v[124:125], v[124:125], v[166:167] op_sel_hi:[1,0]
	v_pk_mul_f32 v[168:169], v[122:123], v[166:167] op_sel_hi:[1,0]
	v_pk_mul_f32 v[122:123], v[120:121], v[166:167] op_sel_hi:[1,0]
	v_cvt_pk_bf16_f32 v120, v124, v125
	v_cvt_pk_bf16_f32 v121, v126, v127
	v_pk_mul_f32 v[116:117], v[116:117], v[166:167] op_sel_hi:[1,0]
	v_cvt_pk_bf16_f32 v122, v122, v123
	v_cvt_pk_bf16_f32 v123, v168, v169
	global_store_dwordx4 v[170:171], v[120:123], off
	v_pk_mul_f32 v[118:119], v[118:119], v[166:167] op_sel_hi:[1,0]
	s_mov_b64 s[72:73], s[24:25]
	v_pk_mul_f32 v[120:121], v[114:115], v[166:167] op_sel_hi:[1,0]
	v_pk_mul_f32 v[114:115], v[112:113], v[166:167] op_sel_hi:[1,0]
	v_cvt_pk_bf16_f32 v112, v116, v117
	v_cvt_pk_bf16_f32 v113, v118, v119
	s_nop 0
	v_cvt_pk_bf16_f32 v114, v114, v115
	v_cvt_pk_bf16_f32 v115, v120, v121
	global_store_dwordx4 v[170:171], v[112:115], off offset:256
	s_nop 1
	v_or_b32_e32 v112, 16, v164
	v_mad_i64_i32 v[116:117], s[8:9], v112, s27, v[144:145]
	ds_read_b128 v[112:115], v165 offset:256
	s_waitcnt lgkmcnt(0)
	v_mov_b32_e32 v118, v113
	v_mov_b32_e32 v119, v114
	v_mov_b32_e32 v113, v115
	v_pk_add_f32 v[112:113], v[118:119], v[112:113]
	s_nop 0
	v_add_f32_e32 v112, v112, v113
	v_fmamk_f32 v112, v112, 0x3a800000, v198
	s_nop 0
	v_rsq_f32_e32 v112, v112
	s_nop 0
	v_mul_f32_e32 v112, v163, v112
	v_pk_mul_f32 v[110:111], v[110:111], v[112:113] op_sel_hi:[1,0]
	v_pk_mul_f32 v[108:109], v[108:109], v[112:113] op_sel_hi:[1,0]
	v_pk_mul_f32 v[114:115], v[106:107], v[112:113] op_sel_hi:[1,0]
	v_pk_mul_f32 v[106:107], v[104:105], v[112:113] op_sel_hi:[1,0]
	v_cvt_pk_bf16_f32 v104, v108, v109
	v_cvt_pk_bf16_f32 v105, v110, v111
	v_pk_mul_f32 v[100:101], v[100:101], v[112:113] op_sel_hi:[1,0]
	v_cvt_pk_bf16_f32 v106, v106, v107
	v_cvt_pk_bf16_f32 v107, v114, v115
	global_store_dwordx4 v[116:117], v[104:107], off
	v_pk_mul_f32 v[102:103], v[102:103], v[112:113] op_sel_hi:[1,0]
	s_nop 0
	v_pk_mul_f32 v[104:105], v[98:99], v[112:113] op_sel_hi:[1,0]
	v_pk_mul_f32 v[98:99], v[96:97], v[112:113] op_sel_hi:[1,0]
	v_cvt_pk_bf16_f32 v96, v100, v101
	v_cvt_pk_bf16_f32 v97, v102, v103
	s_nop 0
	v_cvt_pk_bf16_f32 v98, v98, v99
	v_cvt_pk_bf16_f32 v99, v104, v105
	global_store_dwordx4 v[116:117], v[96:99], off offset:256
	s_nop 1
	v_or_b32_e32 v96, 32, v164
	v_mad_i64_i32 v[100:101], s[8:9], v96, s27, v[144:145]
	ds_read_b128 v[96:99], v165 offset:512
	s_waitcnt lgkmcnt(0)
	v_mov_b32_e32 v102, v97
	v_mov_b32_e32 v103, v98
	v_mov_b32_e32 v97, v99
	v_pk_add_f32 v[96:97], v[102:103], v[96:97]
	s_nop 0
	v_add_f32_e32 v96, v96, v97
	v_fmamk_f32 v96, v96, 0x3a800000, v198
	s_nop 0
	v_rsq_f32_e32 v96, v96
	s_nop 0
	v_mul_f32_e32 v96, v163, v96
	v_pk_mul_f32 v[94:95], v[94:95], v[96:97] op_sel_hi:[1,0]
	v_pk_mul_f32 v[92:93], v[92:93], v[96:97] op_sel_hi:[1,0]
	v_pk_mul_f32 v[98:99], v[90:91], v[96:97] op_sel_hi:[1,0]
	v_pk_mul_f32 v[90:91], v[88:89], v[96:97] op_sel_hi:[1,0]
	v_cvt_pk_bf16_f32 v88, v92, v93
	v_cvt_pk_bf16_f32 v89, v94, v95
	v_pk_mul_f32 v[84:85], v[84:85], v[96:97] op_sel_hi:[1,0]
	v_cvt_pk_bf16_f32 v90, v90, v91
	v_cvt_pk_bf16_f32 v91, v98, v99
	global_store_dwordx4 v[100:101], v[88:91], off
	v_pk_mul_f32 v[86:87], v[86:87], v[96:97] op_sel_hi:[1,0]
	s_nop 0
	v_pk_mul_f32 v[88:89], v[82:83], v[96:97] op_sel_hi:[1,0]
	v_pk_mul_f32 v[82:83], v[80:81], v[96:97] op_sel_hi:[1,0]
	v_cvt_pk_bf16_f32 v80, v84, v85
	v_cvt_pk_bf16_f32 v81, v86, v87
	s_nop 0
	v_cvt_pk_bf16_f32 v82, v82, v83
	v_cvt_pk_bf16_f32 v83, v88, v89
	global_store_dwordx4 v[100:101], v[80:83], off offset:256
	s_nop 1
	v_or_b32_e32 v80, 48, v164
	v_mad_i64_i32 v[84:85], s[8:9], v80, s27, v[144:145]
	ds_read_b128 v[80:83], v165 offset:768
	s_waitcnt lgkmcnt(0)
	v_mov_b32_e32 v86, v81
	v_mov_b32_e32 v87, v82
	v_mov_b32_e32 v81, v83
	v_pk_add_f32 v[80:81], v[86:87], v[80:81]
	s_nop 0
	v_add_f32_e32 v80, v80, v81
	v_fmamk_f32 v80, v80, 0x3a800000, v198
	s_nop 0
	v_rsq_f32_e32 v80, v80
	s_nop 0
	v_mul_f32_e32 v80, v163, v80
	v_pk_mul_f32 v[78:79], v[78:79], v[80:81] op_sel_hi:[1,0]
	v_pk_mul_f32 v[76:77], v[76:77], v[80:81] op_sel_hi:[1,0]
	v_pk_mul_f32 v[82:83], v[74:75], v[80:81] op_sel_hi:[1,0]
	v_pk_mul_f32 v[74:75], v[72:73], v[80:81] op_sel_hi:[1,0]
	v_cvt_pk_bf16_f32 v72, v76, v77
	v_cvt_pk_bf16_f32 v73, v78, v79
	v_pk_mul_f32 v[68:69], v[68:69], v[80:81] op_sel_hi:[1,0]
	v_cvt_pk_bf16_f32 v74, v74, v75
	v_cvt_pk_bf16_f32 v75, v82, v83
	global_store_dwordx4 v[84:85], v[72:75], off
	v_pk_mul_f32 v[70:71], v[70:71], v[80:81] op_sel_hi:[1,0]
	s_nop 0
	v_pk_mul_f32 v[72:73], v[66:67], v[80:81] op_sel_hi:[1,0]
	v_pk_mul_f32 v[66:67], v[64:65], v[80:81] op_sel_hi:[1,0]
	v_cvt_pk_bf16_f32 v64, v68, v69
	v_cvt_pk_bf16_f32 v65, v70, v71
	s_nop 0
	v_cvt_pk_bf16_f32 v66, v66, v67
	v_cvt_pk_bf16_f32 v67, v72, v73
	global_store_dwordx4 v[84:85], v[64:67], off offset:256
	s_nop 1
	v_add_u32_e32 v64, 0x80, v164
	v_mad_i64_i32 v[68:69], s[8:9], v64, s27, v[144:145]
	ds_read_b128 v[64:67], v165 offset:2048
	s_waitcnt lgkmcnt(0)
	v_mov_b32_e32 v70, v65
	v_mov_b32_e32 v71, v66
	v_mov_b32_e32 v65, v67
	v_pk_add_f32 v[64:65], v[70:71], v[64:65]
	s_nop 0
	v_add_f32_e32 v64, v64, v65
	v_fmamk_f32 v64, v64, 0x3a800000, v198
	s_nop 0
	v_rsq_f32_e32 v64, v64
	s_nop 0
	v_mul_f32_e32 v64, v163, v64
	v_pk_mul_f32 v[62:63], v[62:63], v[64:65] op_sel_hi:[1,0]
	v_pk_mul_f32 v[60:61], v[60:61], v[64:65] op_sel_hi:[1,0]
	v_pk_mul_f32 v[66:67], v[58:59], v[64:65] op_sel_hi:[1,0]
	v_pk_mul_f32 v[58:59], v[56:57], v[64:65] op_sel_hi:[1,0]
	v_cvt_pk_bf16_f32 v56, v60, v61
	v_cvt_pk_bf16_f32 v57, v62, v63
	v_pk_mul_f32 v[52:53], v[52:53], v[64:65] op_sel_hi:[1,0]
	v_cvt_pk_bf16_f32 v58, v58, v59
	v_cvt_pk_bf16_f32 v59, v66, v67
	global_store_dwordx4 v[68:69], v[56:59], off
	v_pk_mul_f32 v[54:55], v[54:55], v[64:65] op_sel_hi:[1,0]
	s_nop 0
	v_pk_mul_f32 v[56:57], v[50:51], v[64:65] op_sel_hi:[1,0]
	v_pk_mul_f32 v[50:51], v[48:49], v[64:65] op_sel_hi:[1,0]
	v_cvt_pk_bf16_f32 v48, v52, v53
	v_cvt_pk_bf16_f32 v49, v54, v55
	s_nop 0
	v_cvt_pk_bf16_f32 v50, v50, v51
	v_cvt_pk_bf16_f32 v51, v56, v57
	global_store_dwordx4 v[68:69], v[48:51], off offset:256
	s_nop 1
	v_add_u32_e32 v48, 0x90, v164
	v_mad_i64_i32 v[52:53], s[8:9], v48, s27, v[144:145]
	ds_read_b128 v[48:51], v165 offset:2304
	s_waitcnt lgkmcnt(0)
	v_mov_b32_e32 v54, v49
	v_mov_b32_e32 v55, v50
	v_mov_b32_e32 v49, v51
	v_pk_add_f32 v[48:49], v[54:55], v[48:49]
	s_nop 0
	v_add_f32_e32 v48, v48, v49
	v_fmamk_f32 v48, v48, 0x3a800000, v198
	s_nop 0
	v_rsq_f32_e32 v48, v48
	s_nop 0
	v_mul_f32_e32 v48, v163, v48
	v_pk_mul_f32 v[46:47], v[46:47], v[48:49] op_sel_hi:[1,0]
	v_pk_mul_f32 v[44:45], v[44:45], v[48:49] op_sel_hi:[1,0]
	v_pk_mul_f32 v[50:51], v[42:43], v[48:49] op_sel_hi:[1,0]
	v_pk_mul_f32 v[42:43], v[40:41], v[48:49] op_sel_hi:[1,0]
	v_cvt_pk_bf16_f32 v40, v44, v45
	v_cvt_pk_bf16_f32 v41, v46, v47
	v_pk_mul_f32 v[36:37], v[36:37], v[48:49] op_sel_hi:[1,0]
	v_cvt_pk_bf16_f32 v42, v42, v43
	v_cvt_pk_bf16_f32 v43, v50, v51
	global_store_dwordx4 v[52:53], v[40:43], off
	v_pk_mul_f32 v[38:39], v[38:39], v[48:49] op_sel_hi:[1,0]
	s_nop 0
	v_pk_mul_f32 v[40:41], v[34:35], v[48:49] op_sel_hi:[1,0]
	v_pk_mul_f32 v[34:35], v[32:33], v[48:49] op_sel_hi:[1,0]
	v_cvt_pk_bf16_f32 v32, v36, v37
	v_cvt_pk_bf16_f32 v33, v38, v39
	s_nop 0
	v_cvt_pk_bf16_f32 v34, v34, v35
	v_cvt_pk_bf16_f32 v35, v40, v41
	global_store_dwordx4 v[52:53], v[32:35], off offset:256
	s_nop 1
	v_add_u32_e32 v32, 0xa0, v164
	v_mad_i64_i32 v[36:37], s[8:9], v32, s27, v[144:145]
	ds_read_b128 v[32:35], v165 offset:2560
	s_waitcnt lgkmcnt(0)
	v_mov_b32_e32 v38, v33
	v_mov_b32_e32 v39, v34
	v_mov_b32_e32 v33, v35
	v_pk_add_f32 v[32:33], v[38:39], v[32:33]
	s_nop 0
	v_add_f32_e32 v32, v32, v33
	v_fmamk_f32 v32, v32, 0x3a800000, v198
	s_nop 0
	v_rsq_f32_e32 v32, v32
	s_nop 0
	v_mul_f32_e32 v32, v163, v32
	v_pk_mul_f32 v[30:31], v[30:31], v[32:33] op_sel_hi:[1,0]
	v_pk_mul_f32 v[28:29], v[28:29], v[32:33] op_sel_hi:[1,0]
	v_pk_mul_f32 v[34:35], v[26:27], v[32:33] op_sel_hi:[1,0]
	v_pk_mul_f32 v[26:27], v[24:25], v[32:33] op_sel_hi:[1,0]
	v_cvt_pk_bf16_f32 v24, v28, v29
	v_cvt_pk_bf16_f32 v25, v30, v31
	v_pk_mul_f32 v[20:21], v[20:21], v[32:33] op_sel_hi:[1,0]
	v_cvt_pk_bf16_f32 v26, v26, v27
	v_cvt_pk_bf16_f32 v27, v34, v35
	global_store_dwordx4 v[36:37], v[24:27], off
	v_pk_mul_f32 v[22:23], v[22:23], v[32:33] op_sel_hi:[1,0]
	s_nop 0
	v_pk_mul_f32 v[24:25], v[18:19], v[32:33] op_sel_hi:[1,0]
	v_pk_mul_f32 v[18:19], v[16:17], v[32:33] op_sel_hi:[1,0]
	v_cvt_pk_bf16_f32 v16, v20, v21
	v_cvt_pk_bf16_f32 v17, v22, v23
	s_nop 0
	v_cvt_pk_bf16_f32 v18, v18, v19
	v_cvt_pk_bf16_f32 v19, v24, v25
	global_store_dwordx4 v[36:37], v[16:19], off offset:256
	s_nop 1
	v_add_u32_e32 v16, 0xb0, v164
	v_mad_i64_i32 v[20:21], s[8:9], v16, s27, v[144:145]
	ds_read_b128 v[16:19], v165 offset:2816
	s_waitcnt lgkmcnt(0)
	v_mov_b32_e32 v22, v17
	v_mov_b32_e32 v23, v18
	v_mov_b32_e32 v17, v19
	v_pk_add_f32 v[16:17], v[22:23], v[16:17]
	s_nop 0
	v_add_f32_e32 v16, v16, v17
	v_fmamk_f32 v16, v16, 0x3a800000, v198
	s_nop 0
	v_rsq_f32_e32 v16, v16
	s_nop 0
	v_mul_f32_e32 v16, v163, v16
	v_pk_mul_f32 v[14:15], v[14:15], v[16:17] op_sel_hi:[1,0]
	v_pk_mul_f32 v[12:13], v[12:13], v[16:17] op_sel_hi:[1,0]
	v_pk_mul_f32 v[18:19], v[10:11], v[16:17] op_sel_hi:[1,0]
	v_pk_mul_f32 v[10:11], v[8:9], v[16:17] op_sel_hi:[1,0]
	v_cvt_pk_bf16_f32 v8, v12, v13
	v_cvt_pk_bf16_f32 v9, v14, v15
	s_andn2_b64 vcc, exec, s[46:47]
	v_cvt_pk_bf16_f32 v10, v10, v11
	v_cvt_pk_bf16_f32 v11, v18, v19
	global_store_dwordx4 v[20:21], v[8:11], off
	v_pk_mul_f32 v[6:7], v[6:7], v[16:17] op_sel_hi:[1,0]
	v_pk_mul_f32 v[4:5], v[4:5], v[16:17] op_sel_hi:[1,0]
	v_pk_mul_f32 v[8:9], v[2:3], v[16:17] op_sel_hi:[1,0]
	v_pk_mul_f32 v[2:3], v[0:1], v[16:17] op_sel_hi:[1,0]
	v_cvt_pk_bf16_f32 v0, v4, v5
	v_cvt_pk_bf16_f32 v1, v6, v7
	s_nop 0
	v_cvt_pk_bf16_f32 v2, v2, v3
	v_cvt_pk_bf16_f32 v3, v8, v9
	global_store_dwordx4 v[20:21], v[0:3], off offset:256
	s_cbranch_vccnz .LBB0_263
	s_andn2_b64 vcc, exec, s[20:21]
	s_cbranch_vccnz .LBB0_262
	s_barrier
	s_branch .LBB0_262

.LBB0_298:
	s_add_u32 s100, s53, 0x40080
	s_addc_u32 s101, s27, 0
	v_lshl_add_u64 v[144:145], s[100:101], 0, v[140:141]
	s_add_i32 m0, s60, 0xc000
	s_nop 0
	global_load_lds_dwordx4 v[144:145], off
	v_lshl_add_u64 v[144:145], s[100:101], 0, v[142:143]
	s_add_i32 m0, s60, 0xe000
	s_nop 0
	global_load_lds_dwordx4 v[144:145], off
	v_lshl_or_b32 v144, s8, 8, v159
	s_lshl_b32 s8, s9, 12
	s_and_b32 s8, s8, 0x1000
	v_add_u32_e32 v162, s8, v156
	ds_read_b128 v[164:167], v162
	v_ashrrev_i32_e32 v145, 31, v144
	v_lshl_add_u32 v161, s52, 8, v157
	v_lshl_add_u64 v[144:145], v[144:145], 1, s[74:75]
	v_mad_i64_i32 v[168:169], s[52:53], v161, s11, v[144:145]
	s_waitcnt lgkmcnt(0)
	v_mov_b32_e32 v170, v165
	v_mov_b32_e32 v171, v166
	v_mov_b32_e32 v165, v167
	v_pk_add_f32 v[164:165], v[170:171], v[164:165]
	s_mov_b64 s[52:53], -1
	v_add_f32_e32 v163, v164, v165
	v_fmamk_f32 v163, v163, 0x3a800000, v198
	s_mov_b64 s[72:73], s[24:25]
	v_rsq_f32_e32 v163, v163
	s_nop 0
	v_mov_b32_e32 v164, v163
	v_pk_mul_f32 v[126:127], v[126:127], v[164:165] op_sel_hi:[1,0]
	v_pk_mul_f32 v[124:125], v[124:125], v[164:165] op_sel_hi:[1,0]
	v_pk_mul_f32 v[166:167], v[122:123], v[164:165] op_sel_hi:[1,0]
	v_pk_mul_f32 v[122:123], v[120:121], v[164:165] op_sel_hi:[1,0]
	v_cvt_pk_bf16_f32 v120, v124, v125
	v_cvt_pk_bf16_f32 v121, v126, v127
	v_pk_mul_f32 v[116:117], v[116:117], v[164:165] op_sel_hi:[1,0]
	v_cvt_pk_bf16_f32 v122, v122, v123
	v_cvt_pk_bf16_f32 v123, v166, v167
	global_store_dwordx4 v[168:169], v[120:123], off
	v_pk_mul_f32 v[118:119], v[118:119], v[164:165] op_sel_hi:[1,0]
	s_nop 0
	v_pk_mul_f32 v[120:121], v[114:115], v[164:165] op_sel_hi:[1,0]
	v_pk_mul_f32 v[114:115], v[112:113], v[164:165] op_sel_hi:[1,0]
	v_cvt_pk_bf16_f32 v112, v116, v117
	v_cvt_pk_bf16_f32 v113, v118, v119
	s_nop 0
	v_cvt_pk_bf16_f32 v114, v114, v115
	v_cvt_pk_bf16_f32 v115, v120, v121
	global_store_dwordx4 v[168:169], v[112:115], off offset:256
	s_nop 1
	v_or_b32_e32 v112, 16, v161
	v_mad_i64_i32 v[116:117], s[8:9], v112, s11, v[144:145]
	ds_read_b128 v[112:115], v162 offset:256
	s_waitcnt lgkmcnt(0)
	v_mov_b32_e32 v118, v113
	v_mov_b32_e32 v119, v114
	v_mov_b32_e32 v113, v115
	v_pk_add_f32 v[112:113], v[118:119], v[112:113]
	s_nop 0
	v_add_f32_e32 v112, v112, v113
	v_fmamk_f32 v112, v112, 0x3a800000, v198
	s_nop 0
	v_rsq_f32_e32 v112, v112
	s_nop 0
	v_pk_mul_f32 v[110:111], v[110:111], v[112:113] op_sel_hi:[1,0]
	v_pk_mul_f32 v[108:109], v[108:109], v[112:113] op_sel_hi:[1,0]
	v_pk_mul_f32 v[114:115], v[106:107], v[112:113] op_sel_hi:[1,0]
	v_pk_mul_f32 v[106:107], v[104:105], v[112:113] op_sel_hi:[1,0]
	v_cvt_pk_bf16_f32 v104, v108, v109
	v_cvt_pk_bf16_f32 v105, v110, v111
	v_pk_mul_f32 v[100:101], v[100:101], v[112:113] op_sel_hi:[1,0]
	v_cvt_pk_bf16_f32 v106, v106, v107
	v_cvt_pk_bf16_f32 v107, v114, v115
	global_store_dwordx4 v[116:117], v[104:107], off
	v_pk_mul_f32 v[102:103], v[102:103], v[112:113] op_sel_hi:[1,0]
	s_nop 0
	v_pk_mul_f32 v[104:105], v[98:99], v[112:113] op_sel_hi:[1,0]
	v_pk_mul_f32 v[98:99], v[96:97], v[112:113] op_sel_hi:[1,0]
	v_cvt_pk_bf16_f32 v96, v100, v101
	v_cvt_pk_bf16_f32 v97, v102, v103
	s_nop 0
	v_cvt_pk_bf16_f32 v98, v98, v99
	v_cvt_pk_bf16_f32 v99, v104, v105
	global_store_dwordx4 v[116:117], v[96:99], off offset:256
	s_nop 1
	v_or_b32_e32 v96, 32, v161
	v_mad_i64_i32 v[100:101], s[8:9], v96, s11, v[144:145]
	ds_read_b128 v[96:99], v162 offset:512
	s_waitcnt lgkmcnt(0)
	v_mov_b32_e32 v102, v97
	v_mov_b32_e32 v103, v98
	v_mov_b32_e32 v97, v99
	v_pk_add_f32 v[96:97], v[102:103], v[96:97]
	s_nop 0
	v_add_f32_e32 v96, v96, v97
	v_fmamk_f32 v96, v96, 0x3a800000, v198
	s_nop 0
	v_rsq_f32_e32 v96, v96
	s_nop 0
	v_pk_mul_f32 v[94:95], v[94:95], v[96:97] op_sel_hi:[1,0]
	v_pk_mul_f32 v[92:93], v[92:93], v[96:97] op_sel_hi:[1,0]
	v_pk_mul_f32 v[98:99], v[90:91], v[96:97] op_sel_hi:[1,0]
	v_pk_mul_f32 v[90:91], v[88:89], v[96:97] op_sel_hi:[1,0]
	v_cvt_pk_bf16_f32 v88, v92, v93
	v_cvt_pk_bf16_f32 v89, v94, v95
	v_pk_mul_f32 v[84:85], v[84:85], v[96:97] op_sel_hi:[1,0]
	v_cvt_pk_bf16_f32 v90, v90, v91
	v_cvt_pk_bf16_f32 v91, v98, v99
	global_store_dwordx4 v[100:101], v[88:91], off
	v_pk_mul_f32 v[86:87], v[86:87], v[96:97] op_sel_hi:[1,0]
	s_nop 0
	v_pk_mul_f32 v[88:89], v[82:83], v[96:97] op_sel_hi:[1,0]
	v_pk_mul_f32 v[82:83], v[80:81], v[96:97] op_sel_hi:[1,0]
	v_cvt_pk_bf16_f32 v80, v84, v85
	v_cvt_pk_bf16_f32 v81, v86, v87
	s_nop 0
	v_cvt_pk_bf16_f32 v82, v82, v83
	v_cvt_pk_bf16_f32 v83, v88, v89
	global_store_dwordx4 v[100:101], v[80:83], off offset:256
	s_nop 1
	v_or_b32_e32 v80, 48, v161
	v_mad_i64_i32 v[84:85], s[8:9], v80, s11, v[144:145]
	ds_read_b128 v[80:83], v162 offset:768
	s_waitcnt lgkmcnt(0)
	v_mov_b32_e32 v86, v81
	v_mov_b32_e32 v87, v82
	v_mov_b32_e32 v81, v83
	v_pk_add_f32 v[80:81], v[86:87], v[80:81]
	s_nop 0
	v_add_f32_e32 v80, v80, v81
	v_fmamk_f32 v80, v80, 0x3a800000, v198
	s_nop 0
	v_rsq_f32_e32 v80, v80
	s_nop 0
	v_pk_mul_f32 v[78:79], v[78:79], v[80:81] op_sel_hi:[1,0]
	v_pk_mul_f32 v[76:77], v[76:77], v[80:81] op_sel_hi:[1,0]
	v_pk_mul_f32 v[82:83], v[74:75], v[80:81] op_sel_hi:[1,0]
	v_pk_mul_f32 v[74:75], v[72:73], v[80:81] op_sel_hi:[1,0]
	v_cvt_pk_bf16_f32 v72, v76, v77
	v_cvt_pk_bf16_f32 v73, v78, v79
	v_pk_mul_f32 v[68:69], v[68:69], v[80:81] op_sel_hi:[1,0]
	v_cvt_pk_bf16_f32 v74, v74, v75
	v_cvt_pk_bf16_f32 v75, v82, v83
	global_store_dwordx4 v[84:85], v[72:75], off
	v_pk_mul_f32 v[70:71], v[70:71], v[80:81] op_sel_hi:[1,0]
	s_nop 0
	v_pk_mul_f32 v[72:73], v[66:67], v[80:81] op_sel_hi:[1,0]
	v_pk_mul_f32 v[66:67], v[64:65], v[80:81] op_sel_hi:[1,0]
	v_cvt_pk_bf16_f32 v64, v68, v69
	v_cvt_pk_bf16_f32 v65, v70, v71
	s_nop 0
	v_cvt_pk_bf16_f32 v66, v66, v67
	v_cvt_pk_bf16_f32 v67, v72, v73
	global_store_dwordx4 v[84:85], v[64:67], off offset:256
	s_nop 1
	v_add_u32_e32 v64, 0x80, v161
	v_mad_i64_i32 v[68:69], s[8:9], v64, s11, v[144:145]
	ds_read_b128 v[64:67], v162 offset:2048
	s_waitcnt lgkmcnt(0)
	v_mov_b32_e32 v70, v65
	v_mov_b32_e32 v71, v66
	v_mov_b32_e32 v65, v67
	v_pk_add_f32 v[64:65], v[70:71], v[64:65]
	s_nop 0
	v_add_f32_e32 v64, v64, v65
	v_fmamk_f32 v64, v64, 0x3a800000, v198
	s_nop 0
	v_rsq_f32_e32 v64, v64
	s_nop 0
	v_pk_mul_f32 v[62:63], v[62:63], v[64:65] op_sel_hi:[1,0]
	v_pk_mul_f32 v[60:61], v[60:61], v[64:65] op_sel_hi:[1,0]
	v_pk_mul_f32 v[66:67], v[58:59], v[64:65] op_sel_hi:[1,0]
	v_pk_mul_f32 v[58:59], v[56:57], v[64:65] op_sel_hi:[1,0]
	v_cvt_pk_bf16_f32 v56, v60, v61
	v_cvt_pk_bf16_f32 v57, v62, v63
	v_pk_mul_f32 v[52:53], v[52:53], v[64:65] op_sel_hi:[1,0]
	v_cvt_pk_bf16_f32 v58, v58, v59
	v_cvt_pk_bf16_f32 v59, v66, v67
	global_store_dwordx4 v[68:69], v[56:59], off
	v_pk_mul_f32 v[54:55], v[54:55], v[64:65] op_sel_hi:[1,0]
	s_nop 0
	v_pk_mul_f32 v[56:57], v[50:51], v[64:65] op_sel_hi:[1,0]
	v_pk_mul_f32 v[50:51], v[48:49], v[64:65] op_sel_hi:[1,0]
	v_cvt_pk_bf16_f32 v48, v52, v53
	v_cvt_pk_bf16_f32 v49, v54, v55
	s_nop 0
	v_cvt_pk_bf16_f32 v50, v50, v51
	v_cvt_pk_bf16_f32 v51, v56, v57
	global_store_dwordx4 v[68:69], v[48:51], off offset:256
	s_nop 1
	v_add_u32_e32 v48, 0x90, v161
	v_mad_i64_i32 v[52:53], s[8:9], v48, s11, v[144:145]
	ds_read_b128 v[48:51], v162 offset:2304
	s_waitcnt lgkmcnt(0)
	v_mov_b32_e32 v54, v49
	v_mov_b32_e32 v55, v50
	v_mov_b32_e32 v49, v51
	v_pk_add_f32 v[48:49], v[54:55], v[48:49]
	s_nop 0
	v_add_f32_e32 v48, v48, v49
	v_fmamk_f32 v48, v48, 0x3a800000, v198
	s_nop 0
	v_rsq_f32_e32 v48, v48
	s_nop 0
	v_pk_mul_f32 v[46:47], v[46:47], v[48:49] op_sel_hi:[1,0]
	v_pk_mul_f32 v[44:45], v[44:45], v[48:49] op_sel_hi:[1,0]
	v_pk_mul_f32 v[50:51], v[42:43], v[48:49] op_sel_hi:[1,0]
	v_pk_mul_f32 v[42:43], v[40:41], v[48:49] op_sel_hi:[1,0]
	v_cvt_pk_bf16_f32 v40, v44, v45
	v_cvt_pk_bf16_f32 v41, v46, v47
	v_pk_mul_f32 v[36:37], v[36:37], v[48:49] op_sel_hi:[1,0]
	v_cvt_pk_bf16_f32 v42, v42, v43
	v_cvt_pk_bf16_f32 v43, v50, v51
	global_store_dwordx4 v[52:53], v[40:43], off
	v_pk_mul_f32 v[38:39], v[38:39], v[48:49] op_sel_hi:[1,0]
	s_nop 0
	v_pk_mul_f32 v[40:41], v[34:35], v[48:49] op_sel_hi:[1,0]
	v_pk_mul_f32 v[34:35], v[32:33], v[48:49] op_sel_hi:[1,0]
	v_cvt_pk_bf16_f32 v32, v36, v37
	v_cvt_pk_bf16_f32 v33, v38, v39
	s_nop 0
	v_cvt_pk_bf16_f32 v34, v34, v35
	v_cvt_pk_bf16_f32 v35, v40, v41
	global_store_dwordx4 v[52:53], v[32:35], off offset:256
	s_nop 1
	v_add_u32_e32 v32, 0xa0, v161
	v_mad_i64_i32 v[36:37], s[8:9], v32, s11, v[144:145]
	ds_read_b128 v[32:35], v162 offset:2560
	s_waitcnt lgkmcnt(0)
	v_mov_b32_e32 v38, v33
	v_mov_b32_e32 v39, v34
	v_mov_b32_e32 v33, v35
	v_pk_add_f32 v[32:33], v[38:39], v[32:33]
	s_nop 0
	v_add_f32_e32 v32, v32, v33
	v_fmamk_f32 v32, v32, 0x3a800000, v198
	s_nop 0
	v_rsq_f32_e32 v32, v32
	s_nop 0
	v_pk_mul_f32 v[30:31], v[30:31], v[32:33] op_sel_hi:[1,0]
	v_pk_mul_f32 v[28:29], v[28:29], v[32:33] op_sel_hi:[1,0]
	v_pk_mul_f32 v[34:35], v[26:27], v[32:33] op_sel_hi:[1,0]
	v_pk_mul_f32 v[26:27], v[24:25], v[32:33] op_sel_hi:[1,0]
	v_cvt_pk_bf16_f32 v24, v28, v29
	v_cvt_pk_bf16_f32 v25, v30, v31
	v_pk_mul_f32 v[20:21], v[20:21], v[32:33] op_sel_hi:[1,0]
	v_cvt_pk_bf16_f32 v26, v26, v27
	v_cvt_pk_bf16_f32 v27, v34, v35
	global_store_dwordx4 v[36:37], v[24:27], off
	v_pk_mul_f32 v[22:23], v[22:23], v[32:33] op_sel_hi:[1,0]
	s_nop 0
	v_pk_mul_f32 v[24:25], v[18:19], v[32:33] op_sel_hi:[1,0]
	v_pk_mul_f32 v[18:19], v[16:17], v[32:33] op_sel_hi:[1,0]
	v_cvt_pk_bf16_f32 v16, v20, v21
	v_cvt_pk_bf16_f32 v17, v22, v23
	s_nop 0
	v_cvt_pk_bf16_f32 v18, v18, v19
	v_cvt_pk_bf16_f32 v19, v24, v25
	global_store_dwordx4 v[36:37], v[16:19], off offset:256
	s_nop 1
	v_add_u32_e32 v16, 0xb0, v161
	v_mad_i64_i32 v[20:21], s[8:9], v16, s11, v[144:145]
	ds_read_b128 v[16:19], v162 offset:2816
	s_waitcnt lgkmcnt(0)
	v_mov_b32_e32 v22, v17
	v_mov_b32_e32 v23, v18
	v_mov_b32_e32 v17, v19
	v_pk_add_f32 v[16:17], v[22:23], v[16:17]
	s_nop 0
	v_add_f32_e32 v16, v16, v17
	v_fmamk_f32 v16, v16, 0x3a800000, v198
	s_nop 0
	v_rsq_f32_e32 v16, v16
	s_nop 0
	v_pk_mul_f32 v[14:15], v[14:15], v[16:17] op_sel_hi:[1,0]
	v_pk_mul_f32 v[12:13], v[12:13], v[16:17] op_sel_hi:[1,0]
	v_pk_mul_f32 v[18:19], v[10:11], v[16:17] op_sel_hi:[1,0]
	v_pk_mul_f32 v[10:11], v[8:9], v[16:17] op_sel_hi:[1,0]
	v_cvt_pk_bf16_f32 v8, v12, v13
	v_cvt_pk_bf16_f32 v9, v14, v15
	s_andn2_b64 vcc, exec, s[46:47]
	v_cvt_pk_bf16_f32 v10, v10, v11
	v_cvt_pk_bf16_f32 v11, v18, v19
	global_store_dwordx4 v[20:21], v[8:11], off
	v_pk_mul_f32 v[6:7], v[6:7], v[16:17] op_sel_hi:[1,0]
	v_pk_mul_f32 v[4:5], v[4:5], v[16:17] op_sel_hi:[1,0]
	v_pk_mul_f32 v[8:9], v[2:3], v[16:17] op_sel_hi:[1,0]
	v_pk_mul_f32 v[2:3], v[0:1], v[16:17] op_sel_hi:[1,0]
	v_cvt_pk_bf16_f32 v0, v4, v5
	v_cvt_pk_bf16_f32 v1, v6, v7
	s_nop 0
	v_cvt_pk_bf16_f32 v2, v2, v3
	v_cvt_pk_bf16_f32 v3, v8, v9
	global_store_dwordx4 v[20:21], v[0:3], off offset:256
	s_cbranch_vccnz .LBB0_287
	s_andn2_b64 vcc, exec, s[20:21]
	s_cbranch_vccnz .LBB0_286
	s_barrier
	s_branch .LBB0_286

.LBB0_492:
	v_add_u32_e32 v80, s30, v222
	ds_read_b64_tr_b16 v[112:113], v80 offset:49152
	ds_read_b64_tr_b16 v[114:115], v80 offset:49664
	ds_read_b64_tr_b16 v[116:117], v80 offset:53248
	ds_read_b64_tr_b16 v[118:119], v80 offset:53760
	v_cvt_pk_bf16_f32 v68, v72, v73
	v_cvt_pk_bf16_f32 v69, v74, v75
	v_cvt_pk_bf16_f32 v70, v76, v77
	v_cvt_pk_bf16_f32 v71, v78, v79
	ds_read_b64_tr_b16 v[120:121], v80 offset:57344
	ds_read_b64_tr_b16 v[122:123], v80 offset:57856
	ds_read_b64_tr_b16 v[124:125], v80 offset:61440
	ds_read_b64_tr_b16 v[126:127], v80 offset:61952
	s_waitcnt lgkmcnt(6)
	v_mfma_f32_32x32x16_bf16 v[48:63], v[138:141], v[112:115], v[48:63]
	ds_read_b64_tr_b16 v[112:113], v80 offset:50176
	ds_read_b64_tr_b16 v[114:115], v80 offset:50688
	s_waitcnt lgkmcnt(6)
	v_mfma_f32_32x32x16_bf16 v[32:47], v[138:141], v[116:119], v[32:47]
	ds_read_b64_tr_b16 v[116:117], v80 offset:54272
	ds_read_b64_tr_b16 v[118:119], v80 offset:54784
	s_waitcnt lgkmcnt(6)
	v_mfma_f32_32x32x16_bf16 v[16:31], v[138:141], v[120:123], v[16:31]
	ds_read_b64_tr_b16 v[120:121], v80 offset:58368
	ds_read_b64_tr_b16 v[122:123], v80 offset:58880
	s_waitcnt lgkmcnt(6)
	v_mfma_f32_32x32x16_bf16 v[0:15], v[138:141], v[124:127], v[0:15]
	ds_read_b64_tr_b16 v[124:125], v80 offset:62464
	ds_read_b64_tr_b16 v[126:127], v80 offset:62976
	s_waitcnt lgkmcnt(6)
	v_mfma_f32_32x32x16_bf16 v[48:63], v[134:137], v[112:115], v[48:63]
	ds_read_b64_tr_b16 v[112:113], v80 offset:51200
	ds_read_b64_tr_b16 v[114:115], v80 offset:51712
	s_waitcnt lgkmcnt(6)
	v_mfma_f32_32x32x16_bf16 v[32:47], v[134:137], v[116:119], v[32:47]
	ds_read_b64_tr_b16 v[116:117], v80 offset:55296
	ds_read_b64_tr_b16 v[118:119], v80 offset:55808
	s_waitcnt lgkmcnt(6)
	v_mfma_f32_32x32x16_bf16 v[16:31], v[134:137], v[120:123], v[16:31]
	ds_read_b64_tr_b16 v[120:121], v80 offset:59392
	ds_read_b64_tr_b16 v[122:123], v80 offset:59904
	s_waitcnt lgkmcnt(6)
	v_mfma_f32_32x32x16_bf16 v[0:15], v[134:137], v[124:127], v[0:15]
	ds_read_b64_tr_b16 v[124:125], v80 offset:63488
	ds_read_b64_tr_b16 v[126:127], v80 offset:64000
	s_waitcnt lgkmcnt(6)
	v_mfma_f32_32x32x16_bf16 v[48:63], v[130:133], v[112:115], v[48:63]
	ds_read_b64_tr_b16 v[112:113], v80 offset:52224
	ds_read_b64_tr_b16 v[114:115], v80 offset:52736
	s_waitcnt lgkmcnt(6)
	v_mfma_f32_32x32x16_bf16 v[32:47], v[130:133], v[116:119], v[32:47]
	ds_read_b64_tr_b16 v[116:117], v80 offset:56320
	ds_read_b64_tr_b16 v[118:119], v80 offset:56832
	s_waitcnt lgkmcnt(6)
	v_mfma_f32_32x32x16_bf16 v[16:31], v[130:133], v[120:123], v[16:31]
	ds_read_b64_tr_b16 v[120:121], v80 offset:60416
	ds_read_b64_tr_b16 v[122:123], v80 offset:60928
	s_waitcnt lgkmcnt(6)
	v_mfma_f32_32x32x16_bf16 v[0:15], v[130:133], v[124:127], v[0:15]
	ds_read_b64_tr_b16 v[124:125], v80 offset:64512
	ds_read_b64_tr_b16 v[126:127], v80 offset:65024
	s_waitcnt lgkmcnt(6)
	v_mfma_f32_32x32x16_bf16 v[48:63], v[68:71], v[112:115], v[48:63]
	s_waitcnt lgkmcnt(4)
	v_mfma_f32_32x32x16_bf16 v[32:47], v[68:71], v[116:119], v[32:47]
	s_waitcnt lgkmcnt(2)
	v_mfma_f32_32x32x16_bf16 v[16:31], v[68:71], v[120:123], v[16:31]
	v_add_f32_e32 v64, v76, v77
	v_add_f32_e32 v64, v84, v64
	v_add_f32_e32 v65, v78, v79
	v_add_f32_e32 v64, v65, v64
	v_add_f32_e32 v64, v226, v64
	s_waitcnt lgkmcnt(0)
	v_mfma_f32_32x32x16_bf16 v[0:15], v[68:71], v[124:127], v[0:15]
	s_setprio 0
	v_mov_b32_e32 v65, v64
	v_and_b32_e32 v101, 31, v218
	v_lshlrev_b32_e32 v103, 2, v101
	global_load_dword v100, v103, s[46:47]
	global_load_dword v99, v103, s[46:47] offset:128
	global_load_dword v98, v103, s[46:47] offset:256
	global_load_dword v97, v103, s[46:47] offset:384
	v_and_b32_e32 v96, 63, v218
	v_permlane32_swap_b32_e32 v64, v65
	v_cmp_gt_u32_e32 vcc, 32, v96
	s_and_saveexec_b64 s[20:21], vcc
	v_lshl_add_u32 v66, v101, 2, s67
	v_add_f32_e32 v64, v64, v65
	ds_write_b32 v66, v64 offset:128
	s_or_b64 exec, exec, s[20:21]
	v_lshrrev_b32_e32 v102, 5, v96
	s_waitcnt lgkmcnt(0)
	v_lshl_add_u32 v76, v102, 4, s67
	ds_read_b128 v[64:67], v76 offset:128
	ds_read_b128 v[72:75], v76 offset:160
	v_mov_b32_e32 v68, v48
	s_cmpk_lt_u32 s66, 0x100
	s_cselect_b64 s[20:21], -1, 0
	s_waitcnt lgkmcnt(1)
	v_rcp_f32_e32 v48, v64
	v_cndmask_b32_e64 v108, -v217, 1.0, s[20:21]
	v_mov_b32_e32 v69, v32
	v_mov_b32_e32 v64, v16
	v_mul_f32_e32 v32, v108, v48
	v_rcp_f32_e32 v48, v65
	v_mov_b32_e32 v65, v0
	v_pk_mul_f32 v[92:93], v[68:69], v[32:33] op_sel_hi:[1,0]
	v_pk_mul_f32 v[94:95], v[64:65], v[32:33] op_sel_hi:[1,0]
	v_mul_f32_e32 v16, v108, v48
	v_rcp_f32_e32 v48, v66
	v_mov_b32_e32 v32, v49
	v_mov_b32_e32 v0, v17
	v_pk_mul_f32 v[90:91], v[32:33], v[16:17] op_sel_hi:[1,0]
	v_pk_mul_f32 v[86:87], v[0:1], v[16:17] op_sel_hi:[1,0]
	v_mul_f32_e32 v0, v108, v48
	v_mov_b32_e32 v16, v50
	v_mov_b32_e32 v17, v34
	v_pk_mul_f32 v[80:81], v[16:17], v[0:1] op_sel_hi:[1,0]
	v_rcp_f32_e32 v1, v67
	v_mov_b32_e32 v16, v18
	v_mov_b32_e32 v17, v2
	v_mov_b32_e32 v34, v51
	v_pk_mul_f32 v[82:83], v[16:17], v[0:1] op_sel_hi:[1,0]
	v_mul_f32_e32 v0, v108, v1
	s_waitcnt lgkmcnt(0)
	v_rcp_f32_e32 v1, v72
	v_mov_b32_e32 v2, v19
	s_lshl_b32 s8, s64, 14
	s_add_i32 s8, s8, 0
	v_pk_mul_f32 v[78:79], v[34:35], v[0:1] op_sel_hi:[1,0]
	v_pk_mul_f32 v[18:19], v[2:3], v[0:1] op_sel_hi:[1,0]
	v_mul_f32_e32 v0, v108, v1
	v_mov_b32_e32 v2, v52
	v_mov_b32_e32 v3, v36
	v_pk_mul_f32 v[16:17], v[2:3], v[0:1] op_sel_hi:[1,0]
	v_rcp_f32_e32 v1, v73
	v_mov_b32_e32 v2, v20
	v_mov_b32_e32 v3, v4
	v_mov_b32_e32 v36, v53
	v_pk_mul_f32 v[72:73], v[2:3], v[0:1] op_sel_hi:[1,0]
	v_mul_f32_e32 v0, v108, v1
	v_rcp_f32_e32 v1, v74
	v_mov_b32_e32 v4, v21
	ds_read_b128 v[104:107], v76 offset:224
	v_mov_b32_e32 v34, v22
	v_pk_mul_f32 v[70:71], v[36:37], v[0:1] op_sel_hi:[1,0]
	v_pk_mul_f32 v[20:21], v[4:5], v[0:1] op_sel_hi:[1,0]
	v_mul_f32_e32 v4, v108, v1
	v_mov_b32_e32 v0, v54
	v_mov_b32_e32 v1, v38
	v_pk_mul_f32 v[32:33], v[0:1], v[4:5] op_sel_hi:[1,0]
	ds_read_b128 v[0:3], v76 offset:192
	v_rcp_f32_e32 v5, v75
	v_mov_b32_e32 v35, v6
	v_mov_b32_e32 v38, v55
	v_mov_b32_e32 v6, v23
	s_waitcnt lgkmcnt(0)
	v_rcp_f32_e32 v0, v0
	v_pk_mul_f32 v[34:35], v[34:35], v[4:5] op_sel_hi:[1,0]
	v_mul_f32_e32 v4, v108, v5
	v_pk_mul_f32 v[88:89], v[38:39], v[4:5] op_sel_hi:[1,0]
	v_pk_mul_f32 v[84:85], v[6:7], v[4:5] op_sel_hi:[1,0]
	v_mul_f32_e32 v0, v108, v0
	v_mov_b32_e32 v4, v56
	v_mov_b32_e32 v5, v40
	v_pk_mul_f32 v[76:77], v[4:5], v[0:1] op_sel_hi:[1,0]
	v_rcp_f32_e32 v1, v1
	v_mov_b32_e32 v4, v24
	v_mov_b32_e32 v5, v8
	v_mov_b32_e32 v40, v57
	v_pk_mul_f32 v[74:75], v[4:5], v[0:1] op_sel_hi:[1,0]
	v_mul_f32_e32 v0, v108, v1
	v_rcp_f32_e32 v1, v2
	v_mov_b32_e32 v8, v25
	v_mov_b32_e32 v4, v58
	v_mov_b32_e32 v5, v42
	v_pk_mul_f32 v[38:39], v[40:41], v[0:1] op_sel_hi:[1,0]
	v_pk_mul_f32 v[36:37], v[8:9], v[0:1] op_sel_hi:[1,0]
	v_mul_f32_e32 v0, v108, v1
	v_pk_mul_f32 v[68:69], v[4:5], v[0:1] op_sel_hi:[1,0]
	v_rcp_f32_e32 v1, v3
	v_mov_b32_e32 v2, v26
	v_mov_b32_e32 v3, v10
	v_mov_b32_e32 v42, v59
	v_pk_mul_f32 v[40:41], v[2:3], v[0:1] op_sel_hi:[1,0]
	v_mul_f32_e32 v0, v108, v1
	v_rcp_f32_e32 v1, v104
	v_mov_b32_e32 v10, v27
	v_mov_b32_e32 v2, v60
	v_mov_b32_e32 v3, v44
	v_pk_mul_f32 v[66:67], v[42:43], v[0:1] op_sel_hi:[1,0]
	v_pk_mul_f32 v[50:51], v[10:11], v[0:1] op_sel_hi:[1,0]
	v_mul_f32_e32 v0, v108, v1
	v_pk_mul_f32 v[48:49], v[2:3], v[0:1] op_sel_hi:[1,0]
	v_rcp_f32_e32 v1, v105
	v_mov_b32_e32 v2, v28
	v_mov_b32_e32 v3, v12
	v_mov_b32_e32 v44, v61
	v_pk_mul_f32 v[58:59], v[2:3], v[0:1] op_sel_hi:[1,0]
	v_mul_f32_e32 v0, v108, v1
	v_rcp_f32_e32 v1, v106
	v_mov_b32_e32 v12, v29
	v_mov_b32_e32 v2, v62
	v_mov_b32_e32 v3, v46
	v_pk_mul_f32 v[54:55], v[44:45], v[0:1] op_sel_hi:[1,0]
	v_pk_mul_f32 v[52:53], v[12:13], v[0:1] op_sel_hi:[1,0]
	v_mul_f32_e32 v0, v108, v1
	v_pk_mul_f32 v[56:57], v[2:3], v[0:1] op_sel_hi:[1,0]
	v_rcp_f32_e32 v1, v107
	v_mov_b32_e32 v2, v30
	v_mov_b32_e32 v3, v14
	v_mov_b32_e32 v46, v63
	v_pk_mul_f32 v[64:65], v[2:3], v[0:1] op_sel_hi:[1,0]
	v_mul_f32_e32 v0, v108, v1
	v_mov_b32_e32 v14, v31
	s_waitcnt lgkmcnt(0)
	s_barrier
	v_pk_mul_f32 v[62:63], v[46:47], v[0:1] op_sel_hi:[1,0]
	v_pk_mul_f32 v[60:61], v[14:15], v[0:1] op_sel_hi:[1,0]
	v_lshlrev_b32_e32 v0, 11, v102
	s_cmp_lg_u32 s65, 1
	v_add3_u32 v103, s8, v0, v103
	s_cbranch_scc1 .LBB0_496
	v_add_u32_e32 v0, 0x400, v103
	ds_write2_b32 v103, v92, v93 offset1:32
	ds_write2_b32 v103, v94, v95 offset0:64 offset1:96
	ds_write2_b32 v103, v90, v91 offset0:128 offset1:160
	ds_write2_b32 v103, v86, v87 offset0:192 offset1:224
	ds_write2_b32 v0, v80, v81 offset1:32
	ds_write2_b32 v0, v82, v83 offset0:64 offset1:96
	ds_write2_b32 v0, v78, v79 offset0:128 offset1:160
	ds_write2_b32 v0, v18, v19 offset0:192 offset1:224
	v_add_u32_e32 v0, 0x1000, v103
	ds_write2_b32 v0, v16, v17 offset1:32
	ds_write2_b32 v0, v72, v73 offset0:64 offset1:96
	ds_write2_b32 v0, v70, v71 offset0:128 offset1:160
	ds_write2_b32 v0, v20, v21 offset0:192 offset1:224
	v_add_u32_e32 v0, 0x1400, v103
	ds_write2_b32 v0, v32, v33 offset1:32
	ds_write2_b32 v0, v34, v35 offset0:64 offset1:96
	ds_write2_b32 v0, v88, v89 offset0:128 offset1:160
	ds_write2_b32 v0, v84, v85 offset0:192 offset1:224
	v_add_u32_e32 v0, 0x2000, v103
	ds_write2_b32 v0, v76, v77 offset1:32
	ds_write2_b32 v0, v74, v75 offset0:64 offset1:96
	ds_write2_b32 v0, v38, v39 offset0:128 offset1:160
	ds_write2_b32 v0, v36, v37 offset0:192 offset1:224
	v_add_u32_e32 v0, 0x2400, v103
	ds_write2_b32 v0, v68, v69 offset1:32
	ds_write2_b32 v0, v40, v41 offset0:64 offset1:96
	ds_write2_b32 v0, v66, v67 offset0:128 offset1:160
	ds_write2_b32 v0, v50, v51 offset0:192 offset1:224
	v_add_u32_e32 v0, 0x3000, v103
	ds_write2_b32 v0, v48, v49 offset1:32
	ds_write2_b32 v0, v58, v59 offset0:64 offset1:96
	ds_write2_b32 v0, v54, v55 offset0:128 offset1:160
	ds_write2_b32 v0, v52, v53 offset0:192 offset1:224
	v_add_u32_e32 v0, 0x3400, v103
	ds_write2_b32 v0, v56, v57 offset1:32
	ds_write2_b32 v0, v64, v65 offset0:64 offset1:96
	ds_write2_b32 v0, v62, v63 offset0:128 offset1:160
	ds_write2_b32 v0, v60, v61 offset0:192 offset1:224

.LBB0_1443:
	s_add_u32 s100, s48, 0x40080
	s_addc_u32 s101, s49, 0
	v_lshl_add_u64 v[150:151], s[100:101], 0, v[138:139]
	s_add_i32 m0, s1, 0xc000
	s_nop 0
	global_load_lds_dwordx4 v[150:151], off
	v_lshl_add_u64 v[150:151], s[100:101], 0, v[140:141]
	s_add_i32 m0, s1, 0xe000
	s_nop 0
	global_load_lds_dwordx4 v[150:151], off
	s_lshl_b32 s8, s8, 12
	s_and_b32 s8, s8, 0x1000
	v_add_u32_e32 v144, s8, v164
	ds_read_b128 v[146:149], v144
	s_mov_b32 s8, 0xff61b1e6
	s_waitcnt lgkmcnt(0)
	v_mov_b32_e32 v142, v147
	v_mov_b32_e32 v143, v148
	v_mov_b32_e32 v147, v149
	v_pk_add_f32 v[142:143], v[142:143], v[146:147]
	s_nop 0
	v_add_f32_e32 v142, v142, v143
	v_fmamk_f32 v142, v142, 0x3a800000, v198
	s_nop 0
	v_rsq_f32_e32 v142, v142
	s_nop 0
	v_mov_b32_e32 v143, v142
	v_mul_f32_e32 v142, v124, v143
	v_mul_f32_e32 v145, v125, v143
	v_max3_f32 v142, v142, s8, v145
	v_mul_f32_e32 v145, v126, v143
	v_mul_f32_e32 v146, v127, v143
	v_max3_f32 v142, v142, v145, v146
	v_mul_f32_e32 v145, v120, v143
	v_mul_f32_e32 v146, v121, v143
	v_max3_f32 v142, v142, v145, v146
	v_mul_f32_e32 v145, v122, v143
	v_mul_f32_e32 v146, v123, v143
	v_max3_f32 v142, v142, v145, v146
	v_mul_f32_e32 v145, v116, v143
	v_mul_f32_e32 v146, v117, v143
	v_max3_f32 v142, v142, v145, v146
	v_mul_f32_e32 v145, v118, v143
	v_mul_f32_e32 v146, v119, v143
	v_max3_f32 v142, v142, v145, v146
	v_mul_f32_e32 v145, v112, v143
	v_mul_f32_e32 v146, v113, v143
	v_max3_f32 v142, v142, v145, v146
	v_mul_f32_e32 v145, v114, v143
	v_mul_f32_e32 v146, v115, v143
	v_max3_f32 v142, v142, v145, v146
	v_mov_b32_e32 v145, v142
	s_nop 1
	v_permlane16_swap_b32_e32 v142, v145
	v_max_f32_e32 v145, v145, v145
	v_max_f32_e32 v142, v142, v142
	v_max_f32_e32 v142, v142, v145
	v_mov_b32_e32 v145, v142
	s_nop 1
	v_permlane32_swap_b32_e32 v142, v145
	v_max_f32_e32 v145, v145, v145
	v_max_f32_e32 v142, v142, v142
	v_max_f32_e32 v142, v142, v145
	v_fma_f32 v124, v124, v143, -v142
	v_exp_f32_e32 v124, v124
	v_fma_f32 v125, v125, v143, -v142
	v_exp_f32_e32 v125, v125
	v_fma_f32 v126, v126, v143, -v142
	v_exp_f32_e32 v126, v126
	v_fma_f32 v127, v127, v143, -v142
	v_exp_f32_e32 v127, v127
	v_fma_f32 v120, v120, v143, -v142
	v_add_f32_e32 v145, 0, v124
	v_exp_f32_e32 v120, v120
	v_fma_f32 v121, v121, v143, -v142
	v_add_f32_e32 v145, v125, v145
	v_exp_f32_e32 v121, v121
	v_fma_f32 v122, v122, v143, -v142
	v_add_f32_e32 v145, v126, v145
	v_exp_f32_e32 v122, v122
	v_fma_f32 v123, v123, v143, -v142
	v_add_f32_e32 v145, v127, v145
	v_exp_f32_e32 v123, v123
	v_fma_f32 v116, v116, v143, -v142
	v_add_f32_e32 v145, v120, v145
	v_exp_f32_e32 v116, v116
	v_fma_f32 v117, v117, v143, -v142
	v_add_f32_e32 v145, v121, v145
	v_exp_f32_e32 v117, v117
	v_fma_f32 v118, v118, v143, -v142
	v_add_f32_e32 v145, v122, v145
	v_exp_f32_e32 v118, v118
	v_fma_f32 v119, v119, v143, -v142
	v_add_f32_e32 v145, v123, v145
	v_exp_f32_e32 v119, v119
	v_fma_f32 v112, v112, v143, -v142
	v_add_f32_e32 v145, v116, v145
	v_exp_f32_e32 v112, v112
	v_fma_f32 v113, v113, v143, -v142
	v_add_f32_e32 v145, v117, v145
	v_exp_f32_e32 v113, v113
	v_fma_f32 v114, v114, v143, -v142
	v_add_f32_e32 v145, v118, v145
	v_exp_f32_e32 v114, v114
	v_fma_f32 v115, v115, v143, -v142
	v_add_f32_e32 v145, v119, v145
	v_exp_f32_e32 v115, v115
	v_add_f32_e32 v145, v112, v145
	v_add_f32_e32 v145, v113, v145
	v_add_f32_e32 v145, v114, v145
	v_add_f32_e32 v143, v115, v145
	v_mov_b32_e32 v145, v143
	s_nop 1
	v_permlane16_swap_b32_e32 v143, v145
	v_add_f32_e32 v143, v143, v145
	v_mov_b32_e32 v145, v143
	s_nop 1
	v_permlane32_swap_b32_e32 v143, v145
	s_and_saveexec_b64 s[58:59], s[40:41]
	v_add_f32_e32 v143, v143, v145
	v_add_u32_e32 v145, 0, v155
	v_add_u32_e32 v145, 0x21000, v145
	ds_write_b64 v145, v[142:143]
	s_or_b64 exec, exec, s[58:59]
	ds_read_b128 v[146:149], v144 offset:256
	s_waitcnt lgkmcnt(0)
	v_mov_b32_e32 v142, v147
	v_mov_b32_e32 v143, v148
	v_mov_b32_e32 v147, v149
	v_pk_add_f32 v[142:143], v[142:143], v[146:147]
	s_nop 0
	v_add_f32_e32 v142, v142, v143
	v_fmamk_f32 v142, v142, 0x3a800000, v198
	s_nop 0
	v_rsq_f32_e32 v142, v142
	s_nop 0
	v_mov_b32_e32 v143, v142
	v_mul_f32_e32 v142, v108, v143
	v_mul_f32_e32 v145, v109, v143
	v_max3_f32 v142, v142, s8, v145
	v_mul_f32_e32 v145, v110, v143
	v_mul_f32_e32 v146, v111, v143
	v_max3_f32 v142, v142, v145, v146
	v_mul_f32_e32 v145, v104, v143
	v_mul_f32_e32 v146, v105, v143
	v_max3_f32 v142, v142, v145, v146
	v_mul_f32_e32 v145, v106, v143
	v_mul_f32_e32 v146, v107, v143
	v_max3_f32 v142, v142, v145, v146
	v_mul_f32_e32 v145, v100, v143
	v_mul_f32_e32 v146, v101, v143
	v_max3_f32 v142, v142, v145, v146
	v_mul_f32_e32 v145, v102, v143
	v_mul_f32_e32 v146, v103, v143
	v_max3_f32 v142, v142, v145, v146
	v_mul_f32_e32 v145, v96, v143
	v_mul_f32_e32 v146, v97, v143
	v_max3_f32 v142, v142, v145, v146
	v_mul_f32_e32 v145, v98, v143
	v_mul_f32_e32 v146, v99, v143
	v_max3_f32 v142, v142, v145, v146
	v_mov_b32_e32 v145, v142
	s_nop 1
	v_permlane16_swap_b32_e32 v142, v145
	v_max_f32_e32 v145, v145, v145
	v_max_f32_e32 v142, v142, v142
	v_max_f32_e32 v142, v142, v145
	v_mov_b32_e32 v145, v142
	s_nop 1
	v_permlane32_swap_b32_e32 v142, v145
	v_max_f32_e32 v145, v145, v145
	v_max_f32_e32 v142, v142, v142
	v_max_f32_e32 v142, v142, v145
	v_fma_f32 v108, v108, v143, -v142
	v_exp_f32_e32 v108, v108
	v_fma_f32 v109, v109, v143, -v142
	v_exp_f32_e32 v109, v109
	v_fma_f32 v110, v110, v143, -v142
	v_exp_f32_e32 v110, v110
	v_fma_f32 v111, v111, v143, -v142
	v_exp_f32_e32 v111, v111
	v_fma_f32 v104, v104, v143, -v142
	v_add_f32_e32 v145, 0, v108
	v_exp_f32_e32 v104, v104
	v_fma_f32 v105, v105, v143, -v142
	v_add_f32_e32 v145, v109, v145
	v_exp_f32_e32 v105, v105
	v_fma_f32 v106, v106, v143, -v142
	v_add_f32_e32 v145, v110, v145
	v_exp_f32_e32 v106, v106
	v_fma_f32 v107, v107, v143, -v142
	v_add_f32_e32 v145, v111, v145
	v_exp_f32_e32 v107, v107
	v_fma_f32 v100, v100, v143, -v142
	v_add_f32_e32 v145, v104, v145
	v_exp_f32_e32 v100, v100
	v_fma_f32 v101, v101, v143, -v142
	v_add_f32_e32 v145, v105, v145
	v_exp_f32_e32 v101, v101
	v_fma_f32 v102, v102, v143, -v142
	v_add_f32_e32 v145, v106, v145
	v_exp_f32_e32 v102, v102
	v_fma_f32 v103, v103, v143, -v142
	v_add_f32_e32 v145, v107, v145
	v_exp_f32_e32 v103, v103
	v_fma_f32 v96, v96, v143, -v142
	v_add_f32_e32 v145, v100, v145
	v_exp_f32_e32 v96, v96
	v_fma_f32 v97, v97, v143, -v142
	v_add_f32_e32 v145, v101, v145
	v_exp_f32_e32 v97, v97
	v_fma_f32 v98, v98, v143, -v142
	v_add_f32_e32 v145, v102, v145
	v_exp_f32_e32 v98, v98
	v_fma_f32 v99, v99, v143, -v142
	v_add_f32_e32 v145, v103, v145
	v_exp_f32_e32 v99, v99
	v_add_f32_e32 v145, v96, v145
	v_add_f32_e32 v145, v97, v145
	v_add_f32_e32 v145, v98, v145
	v_add_f32_e32 v143, v99, v145
	v_mov_b32_e32 v145, v143
	s_nop 1
	v_permlane16_swap_b32_e32 v143, v145
	v_add_f32_e32 v143, v143, v145
	v_mov_b32_e32 v145, v143
	s_nop 1
	v_permlane32_swap_b32_e32 v143, v145
	s_and_saveexec_b64 s[58:59], s[40:41]
	v_add_f32_e32 v143, v143, v145
	ds_write_b64 v166, v[142:143]
	s_or_b64 exec, exec, s[58:59]
	ds_read_b128 v[146:149], v144 offset:512
	s_waitcnt lgkmcnt(0)
	v_mov_b32_e32 v142, v147
	v_mov_b32_e32 v143, v148
	v_mov_b32_e32 v147, v149
	v_pk_add_f32 v[142:143], v[142:143], v[146:147]
	s_nop 0
	v_add_f32_e32 v142, v142, v143
	v_fmamk_f32 v142, v142, 0x3a800000, v198
	s_nop 0
	v_rsq_f32_e32 v142, v142
	s_nop 0
	v_mov_b32_e32 v143, v142
	v_mul_f32_e32 v142, v92, v143
	v_mul_f32_e32 v145, v93, v143
	v_max3_f32 v142, v142, s8, v145
	v_mul_f32_e32 v145, v94, v143
	v_mul_f32_e32 v146, v95, v143
	v_max3_f32 v142, v142, v145, v146
	v_mul_f32_e32 v145, v88, v143
	v_mul_f32_e32 v146, v89, v143
	v_max3_f32 v142, v142, v145, v146
	v_mul_f32_e32 v145, v90, v143
	v_mul_f32_e32 v146, v91, v143
	v_max3_f32 v142, v142, v145, v146
	v_mul_f32_e32 v145, v84, v143
	v_mul_f32_e32 v146, v85, v143
	v_max3_f32 v142, v142, v145, v146
	v_mul_f32_e32 v145, v86, v143
	v_mul_f32_e32 v146, v87, v143
	v_max3_f32 v142, v142, v145, v146
	v_mul_f32_e32 v145, v80, v143
	v_mul_f32_e32 v146, v81, v143
	v_max3_f32 v142, v142, v145, v146
	v_mul_f32_e32 v145, v82, v143
	v_mul_f32_e32 v146, v83, v143
	v_max3_f32 v142, v142, v145, v146
	v_mov_b32_e32 v145, v142
	s_nop 1
	v_permlane16_swap_b32_e32 v142, v145
	v_max_f32_e32 v145, v145, v145
	v_max_f32_e32 v142, v142, v142
	v_max_f32_e32 v142, v142, v145
	v_mov_b32_e32 v145, v142
	s_nop 1
	v_permlane32_swap_b32_e32 v142, v145
	v_max_f32_e32 v145, v145, v145
	v_max_f32_e32 v142, v142, v142
	v_max_f32_e32 v142, v142, v145
	v_fma_f32 v92, v92, v143, -v142
	v_exp_f32_e32 v92, v92
	v_fma_f32 v93, v93, v143, -v142
	v_exp_f32_e32 v93, v93
	v_fma_f32 v94, v94, v143, -v142
	v_exp_f32_e32 v94, v94
	v_fma_f32 v95, v95, v143, -v142
	v_exp_f32_e32 v95, v95
	v_fma_f32 v88, v88, v143, -v142
	v_add_f32_e32 v145, 0, v92
	v_exp_f32_e32 v88, v88
	v_fma_f32 v89, v89, v143, -v142
	v_add_f32_e32 v145, v93, v145
	v_exp_f32_e32 v89, v89
	v_fma_f32 v90, v90, v143, -v142
	v_add_f32_e32 v145, v94, v145
	v_exp_f32_e32 v90, v90
	v_fma_f32 v91, v91, v143, -v142
	v_add_f32_e32 v145, v95, v145
	v_exp_f32_e32 v91, v91
	v_fma_f32 v84, v84, v143, -v142
	v_add_f32_e32 v145, v88, v145
	v_exp_f32_e32 v84, v84
	v_fma_f32 v85, v85, v143, -v142
	v_add_f32_e32 v145, v89, v145
	v_exp_f32_e32 v85, v85
	v_fma_f32 v86, v86, v143, -v142
	v_add_f32_e32 v145, v90, v145
	v_exp_f32_e32 v86, v86
	v_fma_f32 v87, v87, v143, -v142
	v_add_f32_e32 v145, v91, v145
	v_exp_f32_e32 v87, v87
	v_fma_f32 v80, v80, v143, -v142
	v_add_f32_e32 v145, v84, v145
	v_exp_f32_e32 v80, v80
	v_fma_f32 v81, v81, v143, -v142
	v_add_f32_e32 v145, v85, v145
	v_exp_f32_e32 v81, v81
	v_fma_f32 v82, v82, v143, -v142
	v_add_f32_e32 v145, v86, v145
	v_exp_f32_e32 v82, v82
	v_fma_f32 v83, v83, v143, -v142
	v_add_f32_e32 v145, v87, v145
	v_exp_f32_e32 v83, v83
	v_add_f32_e32 v145, v80, v145
	v_add_f32_e32 v145, v81, v145
	v_add_f32_e32 v145, v82, v145
	v_add_f32_e32 v143, v83, v145
	v_mov_b32_e32 v145, v143
	s_nop 1
	v_permlane16_swap_b32_e32 v143, v145
	v_add_f32_e32 v143, v143, v145
	v_mov_b32_e32 v145, v143
	s_nop 1
	v_permlane32_swap_b32_e32 v143, v145
	s_and_saveexec_b64 s[58:59], s[40:41]
	v_add_f32_e32 v143, v143, v145
	ds_write_b64 v167, v[142:143]
	s_or_b64 exec, exec, s[58:59]
	ds_read_b128 v[146:149], v144 offset:768
	s_waitcnt lgkmcnt(0)
	v_mov_b32_e32 v142, v147
	v_mov_b32_e32 v143, v148
	v_mov_b32_e32 v147, v149
	v_pk_add_f32 v[142:143], v[142:143], v[146:147]
	s_nop 0
	v_add_f32_e32 v142, v142, v143
	v_fmamk_f32 v142, v142, 0x3a800000, v198
	s_nop 0
	v_rsq_f32_e32 v142, v142
	s_nop 0
	v_mov_b32_e32 v143, v142
	v_mul_f32_e32 v142, v76, v143
	v_mul_f32_e32 v145, v77, v143
	v_max3_f32 v142, v142, s8, v145
	v_mul_f32_e32 v145, v78, v143
	v_mul_f32_e32 v146, v79, v143
	v_max3_f32 v142, v142, v145, v146
	v_mul_f32_e32 v145, v72, v143
	v_mul_f32_e32 v146, v73, v143
	v_max3_f32 v142, v142, v145, v146
	v_mul_f32_e32 v145, v74, v143
	v_mul_f32_e32 v146, v75, v143
	v_max3_f32 v142, v142, v145, v146
	v_mul_f32_e32 v145, v68, v143
	v_mul_f32_e32 v146, v69, v143
	v_max3_f32 v142, v142, v145, v146
	v_mul_f32_e32 v145, v70, v143
	v_mul_f32_e32 v146, v71, v143
	v_max3_f32 v142, v142, v145, v146
	v_mul_f32_e32 v145, v64, v143
	v_mul_f32_e32 v146, v65, v143
	v_max3_f32 v142, v142, v145, v146
	v_mul_f32_e32 v145, v66, v143
	v_mul_f32_e32 v146, v67, v143
	v_max3_f32 v142, v142, v145, v146
	v_mov_b32_e32 v145, v142
	s_nop 1
	v_permlane16_swap_b32_e32 v142, v145
	v_max_f32_e32 v145, v145, v145
	v_max_f32_e32 v142, v142, v142
	v_max_f32_e32 v142, v142, v145
	v_mov_b32_e32 v145, v142
	s_nop 1
	v_permlane32_swap_b32_e32 v142, v145
	v_max_f32_e32 v145, v145, v145
	v_max_f32_e32 v142, v142, v142
	v_max_f32_e32 v142, v142, v145
	v_fma_f32 v76, v76, v143, -v142
	v_exp_f32_e32 v76, v76
	v_fma_f32 v77, v77, v143, -v142
	v_exp_f32_e32 v77, v77
	v_fma_f32 v78, v78, v143, -v142
	v_exp_f32_e32 v78, v78
	v_fma_f32 v79, v79, v143, -v142
	v_exp_f32_e32 v79, v79
	v_fma_f32 v72, v72, v143, -v142
	v_add_f32_e32 v145, 0, v76
	v_exp_f32_e32 v72, v72
	v_fma_f32 v73, v73, v143, -v142
	v_add_f32_e32 v145, v77, v145
	v_exp_f32_e32 v73, v73
	v_fma_f32 v74, v74, v143, -v142
	v_add_f32_e32 v145, v78, v145
	v_exp_f32_e32 v74, v74
	v_fma_f32 v75, v75, v143, -v142
	v_add_f32_e32 v145, v79, v145
	v_exp_f32_e32 v75, v75
	v_fma_f32 v68, v68, v143, -v142
	v_add_f32_e32 v145, v72, v145
	v_exp_f32_e32 v68, v68
	v_fma_f32 v69, v69, v143, -v142
	v_add_f32_e32 v145, v73, v145
	v_exp_f32_e32 v69, v69
	v_fma_f32 v70, v70, v143, -v142
	v_add_f32_e32 v145, v74, v145
	v_exp_f32_e32 v70, v70
	v_fma_f32 v71, v71, v143, -v142
	v_add_f32_e32 v145, v75, v145
	v_exp_f32_e32 v71, v71
	v_fma_f32 v64, v64, v143, -v142
	v_add_f32_e32 v145, v68, v145
	v_exp_f32_e32 v64, v64
	v_fma_f32 v65, v65, v143, -v142
	v_add_f32_e32 v145, v69, v145
	v_exp_f32_e32 v65, v65
	v_fma_f32 v66, v66, v143, -v142
	v_add_f32_e32 v145, v70, v145
	v_exp_f32_e32 v66, v66
	v_fma_f32 v67, v67, v143, -v142
	v_add_f32_e32 v145, v71, v145
	v_exp_f32_e32 v67, v67
	v_add_f32_e32 v145, v64, v145
	v_add_f32_e32 v145, v65, v145
	v_add_f32_e32 v145, v66, v145
	v_add_f32_e32 v143, v67, v145
	v_mov_b32_e32 v145, v143
	s_nop 1
	v_permlane16_swap_b32_e32 v143, v145
	v_add_f32_e32 v143, v143, v145
	v_mov_b32_e32 v145, v143
	s_nop 1
	v_permlane32_swap_b32_e32 v143, v145
	s_and_saveexec_b64 s[58:59], s[40:41]
	v_add_f32_e32 v143, v143, v145
	ds_write_b64 v168, v[142:143]
	s_or_b64 exec, exec, s[58:59]
	ds_read_b128 v[146:149], v144 offset:2048
	s_waitcnt lgkmcnt(0)
	v_mov_b32_e32 v142, v147
	v_mov_b32_e32 v143, v148
	v_mov_b32_e32 v147, v149
	v_pk_add_f32 v[142:143], v[142:143], v[146:147]
	s_nop 0
	v_add_f32_e32 v142, v142, v143
	v_fmamk_f32 v142, v142, 0x3a800000, v198
	s_nop 0
	v_rsq_f32_e32 v142, v142
	s_nop 0
	v_mov_b32_e32 v143, v142
	v_mul_f32_e32 v142, v60, v143
	v_mul_f32_e32 v145, v61, v143
	v_max3_f32 v142, v142, s8, v145
	v_mul_f32_e32 v145, v62, v143
	v_mul_f32_e32 v146, v63, v143
	v_max3_f32 v142, v142, v145, v146
	v_mul_f32_e32 v145, v56, v143
	v_mul_f32_e32 v146, v57, v143
	v_max3_f32 v142, v142, v145, v146
	v_mul_f32_e32 v145, v58, v143
	v_mul_f32_e32 v146, v59, v143
	v_max3_f32 v142, v142, v145, v146
	v_mul_f32_e32 v145, v52, v143
	v_mul_f32_e32 v146, v53, v143
	v_max3_f32 v142, v142, v145, v146
	v_mul_f32_e32 v145, v54, v143
	v_mul_f32_e32 v146, v55, v143
	v_max3_f32 v142, v142, v145, v146
	v_mul_f32_e32 v145, v48, v143
	v_mul_f32_e32 v146, v49, v143
	v_max3_f32 v142, v142, v145, v146
	v_mul_f32_e32 v145, v50, v143
	v_mul_f32_e32 v146, v51, v143
	v_max3_f32 v142, v142, v145, v146
	v_mov_b32_e32 v145, v142
	s_nop 1
	v_permlane16_swap_b32_e32 v142, v145
	v_max_f32_e32 v145, v145, v145
	v_max_f32_e32 v142, v142, v142
	v_max_f32_e32 v142, v142, v145
	v_mov_b32_e32 v145, v142
	s_nop 1
	v_permlane32_swap_b32_e32 v142, v145
	v_max_f32_e32 v145, v145, v145
	v_max_f32_e32 v142, v142, v142
	v_max_f32_e32 v142, v142, v145
	v_fma_f32 v60, v60, v143, -v142
	v_exp_f32_e32 v60, v60
	v_fma_f32 v61, v61, v143, -v142
	v_exp_f32_e32 v61, v61
	v_fma_f32 v62, v62, v143, -v142
	v_exp_f32_e32 v62, v62
	v_fma_f32 v63, v63, v143, -v142
	v_exp_f32_e32 v63, v63
	v_fma_f32 v56, v56, v143, -v142
	v_add_f32_e32 v145, 0, v60
	v_exp_f32_e32 v56, v56
	v_fma_f32 v57, v57, v143, -v142
	v_add_f32_e32 v145, v61, v145
	v_exp_f32_e32 v57, v57
	v_fma_f32 v58, v58, v143, -v142
	v_add_f32_e32 v145, v62, v145
	v_exp_f32_e32 v58, v58
	v_fma_f32 v59, v59, v143, -v142
	v_add_f32_e32 v145, v63, v145
	v_exp_f32_e32 v59, v59
	v_fma_f32 v52, v52, v143, -v142
	v_add_f32_e32 v145, v56, v145
	v_exp_f32_e32 v52, v52
	v_fma_f32 v53, v53, v143, -v142
	v_add_f32_e32 v145, v57, v145
	v_exp_f32_e32 v53, v53
	v_fma_f32 v54, v54, v143, -v142
	v_add_f32_e32 v145, v58, v145
	v_exp_f32_e32 v54, v54
	v_fma_f32 v55, v55, v143, -v142
	v_add_f32_e32 v145, v59, v145
	v_exp_f32_e32 v55, v55
	v_fma_f32 v48, v48, v143, -v142
	v_add_f32_e32 v145, v52, v145
	v_exp_f32_e32 v48, v48
	v_fma_f32 v49, v49, v143, -v142
	v_add_f32_e32 v145, v53, v145
	v_exp_f32_e32 v49, v49
	v_fma_f32 v50, v50, v143, -v142
	v_add_f32_e32 v145, v54, v145
	v_exp_f32_e32 v50, v50
	v_fma_f32 v51, v51, v143, -v142
	v_add_f32_e32 v145, v55, v145
	v_exp_f32_e32 v51, v51
	v_add_f32_e32 v145, v48, v145
	v_add_f32_e32 v145, v49, v145
	v_add_f32_e32 v145, v50, v145
	v_add_f32_e32 v143, v51, v145
	v_mov_b32_e32 v145, v143
	s_nop 1
	v_permlane16_swap_b32_e32 v143, v145
	v_add_f32_e32 v143, v143, v145
	v_mov_b32_e32 v145, v143
	s_nop 1
	v_permlane32_swap_b32_e32 v143, v145
	s_and_saveexec_b64 s[58:59], s[40:41]
	v_add_f32_e32 v143, v143, v145
	ds_write_b64 v169, v[142:143]
	s_or_b64 exec, exec, s[58:59]
	ds_read_b128 v[146:149], v144 offset:2304
	s_waitcnt lgkmcnt(0)
	v_mov_b32_e32 v142, v147
	v_mov_b32_e32 v143, v148
	v_mov_b32_e32 v147, v149
	v_pk_add_f32 v[142:143], v[142:143], v[146:147]
	s_nop 0
	v_add_f32_e32 v142, v142, v143
	v_fmamk_f32 v142, v142, 0x3a800000, v198
	s_nop 0
	v_rsq_f32_e32 v142, v142
	s_nop 0
	v_mov_b32_e32 v143, v142
	v_mul_f32_e32 v142, v44, v143
	v_mul_f32_e32 v145, v45, v143
	v_max3_f32 v142, v142, s8, v145
	v_mul_f32_e32 v145, v46, v143
	v_mul_f32_e32 v146, v47, v143
	v_max3_f32 v142, v142, v145, v146
	v_mul_f32_e32 v145, v40, v143
	v_mul_f32_e32 v146, v41, v143
	v_max3_f32 v142, v142, v145, v146
	v_mul_f32_e32 v145, v42, v143
	v_mul_f32_e32 v146, v43, v143
	v_max3_f32 v142, v142, v145, v146
	v_mul_f32_e32 v145, v36, v143
	v_mul_f32_e32 v146, v37, v143
	v_max3_f32 v142, v142, v145, v146
	v_mul_f32_e32 v145, v38, v143
	v_mul_f32_e32 v146, v39, v143
	v_max3_f32 v142, v142, v145, v146
	v_mul_f32_e32 v145, v32, v143
	v_mul_f32_e32 v146, v33, v143
	v_max3_f32 v142, v142, v145, v146
	v_mul_f32_e32 v145, v34, v143
	v_mul_f32_e32 v146, v35, v143
	v_max3_f32 v142, v142, v145, v146
	v_mov_b32_e32 v145, v142
	s_nop 1
	v_permlane16_swap_b32_e32 v142, v145
	v_max_f32_e32 v145, v145, v145
	v_max_f32_e32 v142, v142, v142
	v_max_f32_e32 v142, v142, v145
	v_mov_b32_e32 v145, v142
	s_nop 1
	v_permlane32_swap_b32_e32 v142, v145
	v_max_f32_e32 v145, v145, v145
	v_max_f32_e32 v142, v142, v142
	v_max_f32_e32 v142, v142, v145
	v_fma_f32 v44, v44, v143, -v142
	v_exp_f32_e32 v44, v44
	v_fma_f32 v45, v45, v143, -v142
	v_exp_f32_e32 v45, v45
	v_fma_f32 v46, v46, v143, -v142
	v_exp_f32_e32 v46, v46
	v_fma_f32 v47, v47, v143, -v142
	v_exp_f32_e32 v47, v47
	v_fma_f32 v40, v40, v143, -v142
	v_add_f32_e32 v145, 0, v44
	v_exp_f32_e32 v40, v40
	v_fma_f32 v41, v41, v143, -v142
	v_add_f32_e32 v145, v45, v145
	v_exp_f32_e32 v41, v41
	v_fma_f32 v42, v42, v143, -v142
	v_add_f32_e32 v145, v46, v145
	v_exp_f32_e32 v42, v42
	v_fma_f32 v43, v43, v143, -v142
	v_add_f32_e32 v145, v47, v145
	v_exp_f32_e32 v43, v43
	v_fma_f32 v36, v36, v143, -v142
	v_add_f32_e32 v145, v40, v145
	v_exp_f32_e32 v36, v36
	v_fma_f32 v37, v37, v143, -v142
	v_add_f32_e32 v145, v41, v145
	v_exp_f32_e32 v37, v37
	v_fma_f32 v38, v38, v143, -v142
	v_add_f32_e32 v145, v42, v145
	v_exp_f32_e32 v38, v38
	v_fma_f32 v39, v39, v143, -v142
	v_add_f32_e32 v145, v43, v145
	v_exp_f32_e32 v39, v39
	v_fma_f32 v32, v32, v143, -v142
	v_add_f32_e32 v145, v36, v145
	v_exp_f32_e32 v32, v32
	v_fma_f32 v33, v33, v143, -v142
	v_add_f32_e32 v145, v37, v145
	v_exp_f32_e32 v33, v33
	v_fma_f32 v34, v34, v143, -v142
	v_add_f32_e32 v145, v38, v145
	v_exp_f32_e32 v34, v34
	v_fma_f32 v35, v35, v143, -v142
	v_add_f32_e32 v145, v39, v145
	v_exp_f32_e32 v35, v35
	v_add_f32_e32 v145, v32, v145
	v_add_f32_e32 v145, v33, v145
	v_add_f32_e32 v145, v34, v145
	v_add_f32_e32 v143, v35, v145
	v_mov_b32_e32 v145, v143
	s_nop 1
	v_permlane16_swap_b32_e32 v143, v145
	v_add_f32_e32 v143, v143, v145
	v_mov_b32_e32 v145, v143
	s_nop 1
	v_permlane32_swap_b32_e32 v143, v145
	s_and_saveexec_b64 s[58:59], s[40:41]
	v_add_f32_e32 v143, v143, v145
	ds_write_b64 v170, v[142:143]
	s_or_b64 exec, exec, s[58:59]
	ds_read_b128 v[146:149], v144 offset:2560
	s_waitcnt lgkmcnt(0)
	v_mov_b32_e32 v142, v147
	v_mov_b32_e32 v143, v148
	v_mov_b32_e32 v147, v149
	v_pk_add_f32 v[142:143], v[142:143], v[146:147]
	s_nop 0
	v_add_f32_e32 v142, v142, v143
	v_fmamk_f32 v142, v142, 0x3a800000, v198
	s_nop 0
	v_rsq_f32_e32 v142, v142
	s_nop 0
	v_mov_b32_e32 v143, v142
	v_mul_f32_e32 v142, v28, v143
	v_mul_f32_e32 v145, v29, v143
	v_max3_f32 v142, v142, s8, v145
	v_mul_f32_e32 v145, v30, v143
	v_mul_f32_e32 v146, v31, v143
	v_max3_f32 v142, v142, v145, v146
	v_mul_f32_e32 v145, v24, v143
	v_mul_f32_e32 v146, v25, v143
	v_max3_f32 v142, v142, v145, v146
	v_mul_f32_e32 v145, v26, v143
	v_mul_f32_e32 v146, v27, v143
	v_max3_f32 v142, v142, v145, v146
	v_mul_f32_e32 v145, v20, v143
	v_mul_f32_e32 v146, v21, v143
	v_max3_f32 v142, v142, v145, v146
	v_mul_f32_e32 v145, v22, v143
	v_mul_f32_e32 v146, v23, v143
	v_max3_f32 v142, v142, v145, v146
	v_mul_f32_e32 v145, v16, v143
	v_mul_f32_e32 v146, v17, v143
	v_max3_f32 v142, v142, v145, v146
	v_mul_f32_e32 v145, v18, v143
	v_mul_f32_e32 v146, v19, v143
	v_max3_f32 v142, v142, v145, v146
	v_mov_b32_e32 v145, v142
	s_nop 1
	v_permlane16_swap_b32_e32 v142, v145
	v_max_f32_e32 v145, v145, v145
	v_max_f32_e32 v142, v142, v142
	v_max_f32_e32 v142, v142, v145
	v_mov_b32_e32 v145, v142
	s_nop 1
	v_permlane32_swap_b32_e32 v142, v145
	v_max_f32_e32 v145, v145, v145
	v_max_f32_e32 v142, v142, v142
	v_max_f32_e32 v142, v142, v145
	v_fma_f32 v28, v28, v143, -v142
	v_exp_f32_e32 v28, v28
	v_fma_f32 v29, v29, v143, -v142
	v_exp_f32_e32 v29, v29
	v_fma_f32 v30, v30, v143, -v142
	v_exp_f32_e32 v30, v30
	v_fma_f32 v31, v31, v143, -v142
	v_exp_f32_e32 v31, v31
	v_fma_f32 v24, v24, v143, -v142
	v_add_f32_e32 v145, 0, v28
	v_exp_f32_e32 v24, v24
	v_fma_f32 v25, v25, v143, -v142
	v_add_f32_e32 v145, v29, v145
	v_exp_f32_e32 v25, v25
	v_fma_f32 v26, v26, v143, -v142
	v_add_f32_e32 v145, v30, v145
	v_exp_f32_e32 v26, v26
	v_fma_f32 v27, v27, v143, -v142
	v_add_f32_e32 v145, v31, v145
	v_exp_f32_e32 v27, v27
	v_fma_f32 v20, v20, v143, -v142
	v_add_f32_e32 v145, v24, v145
	v_exp_f32_e32 v20, v20
	v_fma_f32 v21, v21, v143, -v142
	v_add_f32_e32 v145, v25, v145
	v_exp_f32_e32 v21, v21
	v_fma_f32 v22, v22, v143, -v142
	v_add_f32_e32 v145, v26, v145
	v_exp_f32_e32 v22, v22
	v_fma_f32 v23, v23, v143, -v142
	v_add_f32_e32 v145, v27, v145
	v_exp_f32_e32 v23, v23
	v_fma_f32 v16, v16, v143, -v142
	v_add_f32_e32 v145, v20, v145
	v_exp_f32_e32 v16, v16
	v_fma_f32 v17, v17, v143, -v142
	v_add_f32_e32 v145, v21, v145
	v_exp_f32_e32 v17, v17
	v_fma_f32 v18, v18, v143, -v142
	v_add_f32_e32 v145, v22, v145
	v_exp_f32_e32 v18, v18
	v_fma_f32 v19, v19, v143, -v142
	v_add_f32_e32 v145, v23, v145
	v_exp_f32_e32 v19, v19
	v_add_f32_e32 v145, v16, v145
	v_add_f32_e32 v145, v17, v145
	v_add_f32_e32 v145, v18, v145
	v_add_f32_e32 v143, v19, v145
	v_mov_b32_e32 v145, v143
	s_nop 1
	v_permlane16_swap_b32_e32 v143, v145
	v_add_f32_e32 v143, v143, v145
	v_mov_b32_e32 v145, v143
	s_nop 1
	v_permlane32_swap_b32_e32 v143, v145
	s_and_saveexec_b64 s[58:59], s[40:41]
	v_add_f32_e32 v143, v143, v145
	ds_write_b64 v171, v[142:143]
	s_or_b64 exec, exec, s[58:59]
	ds_read_b128 v[142:145], v144 offset:2816
	s_waitcnt lgkmcnt(0)
	v_mov_b32_e32 v146, v143
	v_mov_b32_e32 v147, v144
	v_mov_b32_e32 v143, v145
	v_pk_add_f32 v[142:143], v[146:147], v[142:143]
	s_nop 0
	v_add_f32_e32 v142, v142, v143
	v_fmamk_f32 v142, v142, 0x3a800000, v198
	s_nop 0
	v_rsq_f32_e32 v142, v142
	s_nop 0
	v_mov_b32_e32 v149, v142
	v_mul_f32_e32 v142, v12, v149
	v_mul_f32_e32 v143, v13, v149
	v_max3_f32 v142, v142, s8, v143
	v_mul_f32_e32 v143, v14, v149
	v_mul_f32_e32 v144, v15, v149
	v_max3_f32 v142, v142, v143, v144
	v_mul_f32_e32 v143, v8, v149
	v_mul_f32_e32 v144, v9, v149
	v_max3_f32 v142, v142, v143, v144
	v_mul_f32_e32 v143, v10, v149
	v_mul_f32_e32 v144, v11, v149
	v_max3_f32 v142, v142, v143, v144
	v_mul_f32_e32 v143, v4, v149
	v_mul_f32_e32 v144, v5, v149
	v_max3_f32 v142, v142, v143, v144
	v_mul_f32_e32 v143, v6, v149
	v_mul_f32_e32 v144, v7, v149
	v_max3_f32 v142, v142, v143, v144
	v_mul_f32_e32 v143, v0, v149
	v_mul_f32_e32 v144, v1, v149
	v_max3_f32 v142, v142, v143, v144
	v_mul_f32_e32 v143, v2, v149
	v_mul_f32_e32 v144, v3, v149
	v_max3_f32 v142, v142, v143, v144
	v_mov_b32_e32 v143, v142
	s_nop 1
	v_permlane16_swap_b32_e32 v142, v143
	v_max_f32_e32 v143, v143, v143
	v_max_f32_e32 v142, v142, v142
	v_max_f32_e32 v142, v142, v143
	v_mov_b32_e32 v143, v142
	s_nop 1
	v_permlane32_swap_b32_e32 v142, v143
	v_max_f32_e32 v143, v143, v143
	v_max_f32_e32 v142, v142, v142
	v_max_f32_e32 v150, v142, v143
	v_fma_f32 v12, v12, v149, -v150
	v_exp_f32_e32 v12, v12
	v_fma_f32 v13, v13, v149, -v150
	v_exp_f32_e32 v13, v13
	v_fma_f32 v14, v14, v149, -v150
	v_exp_f32_e32 v14, v14
	v_fma_f32 v15, v15, v149, -v150
	v_exp_f32_e32 v15, v15
	v_fma_f32 v8, v8, v149, -v150
	v_add_f32_e32 v142, 0, v12
	v_exp_f32_e32 v8, v8
	v_fma_f32 v9, v9, v149, -v150
	v_add_f32_e32 v142, v13, v142
	v_exp_f32_e32 v9, v9
	v_add_f32_e32 v142, v14, v142
	v_add_f32_e32 v142, v15, v142
	v_add_f32_e32 v142, v8, v142
	v_fma_f32 v10, v10, v149, -v150
	v_add_f32_e32 v143, v9, v142
	v_exp_f32_e32 v142, v10
	v_fma_f32 v11, v11, v149, -v150
	v_fma_f32 v4, v4, v149, -v150
	v_fma_f32 v5, v5, v149, -v150
	v_add_f32_e32 v10, v142, v143
	v_exp_f32_e32 v143, v11
	v_fma_f32 v0, v0, v149, -v150
	v_exp_f32_e32 v146, v0
	v_fma_f32 v1, v1, v149, -v150
	v_add_f32_e32 v11, v143, v10
	v_exp_f32_e32 v10, v4
	v_exp_f32_e32 v147, v1
	v_fma_f32 v1, v2, v149, -v150
	v_exp_f32_e32 v148, v1
	v_add_f32_e32 v4, v10, v11
	v_exp_f32_e32 v11, v5
	v_fma_f32 v5, v6, v149, -v150
	v_exp_f32_e32 v144, v5
	v_fma_f32 v5, v7, v149, -v150
	v_exp_f32_e32 v145, v5
	v_add_f32_e32 v4, v11, v4
	v_add_f32_e32 v4, v144, v4
	v_fma_f32 v1, v3, v149, -v150
	v_add_f32_e32 v4, v145, v4
	v_exp_f32_e32 v149, v1
	v_add_f32_e32 v0, v146, v4
	v_add_f32_e32 v0, v147, v0
	v_add_f32_e32 v0, v148, v0
	v_add_f32_e32 v0, v149, v0
	v_mov_b32_e32 v1, v0
	s_nop 1
	v_permlane16_swap_b32_e32 v0, v1
	v_add_f32_e32 v0, v0, v1
	v_mov_b32_e32 v1, v0
	s_nop 1
	v_permlane32_swap_b32_e32 v0, v1
	s_and_saveexec_b64 s[58:59], s[40:41]
	v_add_f32_e32 v151, v0, v1
	ds_write_b64 v172, v[150:151]
	s_or_b64 exec, exec, s[58:59]
	s_waitcnt lgkmcnt(0)
	s_barrier
	ds_read_b128 v[0:3], v173 offset:16
	ds_read_b128 v[4:7], v173
	s_cmp_lt_i32 s66, 1
	s_waitcnt lgkmcnt(0)
	v_max_f32_e32 v150, v2, v2
	v_max_f32_e32 v151, v0, v0
	v_max_f32_e32 v150, v151, v150
	v_max3_f32 v150, v4, v6, v150
	v_sub_f32_e32 v4, v4, v150
	v_exp_f32_e32 v4, v4
	v_sub_f32_e32 v6, v6, v150
	v_exp_f32_e32 v6, v6
	v_mov_b32_e32 v181, v4
	s_cbranch_scc1 .LBB0_1464
	s_cmp_lg_u32 s66, 1
	s_mov_b64 s[58:59], -1
	s_cbranch_scc0 .LBB0_1462
	v_cndmask_b32_e64 v151, v2, v0, s[42:43]
	v_sub_f32_e32 v151, v151, v150
	v_exp_f32_e32 v181, v151
	s_mov_b64 s[58:59], 0

.LBB0_1692:
	s_add_u32 s100, s53, 0x40080
	s_addc_u32 s101, s45, 0
	v_lshl_add_u64 v[146:147], s[100:101], 0, v[138:139]
	s_add_i32 m0, s1, 0xc000
	s_nop 0
	global_load_lds_dwordx4 v[146:147], off
	v_lshl_add_u64 v[146:147], s[100:101], 0, v[140:141]
	s_add_i32 m0, s1, 0xe000
	s_nop 0
	global_load_lds_dwordx4 v[146:147], off
	s_lshl_b32 s9, s9, 12
	s_and_b32 s9, s9, 0x1000
	v_add_u32_e32 v154, s9, v151
	ds_read_b128 v[156:159], v154
	v_lshl_or_b32 v142, s8, 8, v152
	v_ashrrev_i32_e32 v143, 31, v142
	v_lshl_add_u64 v[144:145], v[142:143], 1, s[74:75]
	v_lshl_add_u32 v146, s52, 8, v148
	s_waitcnt lgkmcnt(0)
	v_mov_b32_e32 v142, v157
	v_mov_b32_e32 v143, v158
	v_mov_b32_e32 v157, v159
	v_pk_add_f32 v[142:143], v[142:143], v[156:157]
	v_ashrrev_i32_e32 v147, 31, v146
	v_add_f32_e32 v142, v142, v143
	v_fmamk_f32 v142, v142, 0x3a800000, v198
	s_mov_b32 s8, 0x100000
	s_mov_b64 s[72:73], s[24:25]
	v_rsq_f32_e32 v155, v142
	v_lshlrev_b64 v[142:143], 13, v[146:147]
	v_lshl_add_u64 v[142:143], v[144:145], 0, v[142:143]
	v_mov_b32_e32 v156, v155
	v_pk_mul_f32 v[120:121], v[120:121], v[156:157] op_sel_hi:[1,0]
	v_pk_mul_f32 v[124:125], v[124:125], v[156:157] op_sel_hi:[1,0]
	v_pk_mul_f32 v[122:123], v[122:123], v[156:157] op_sel_hi:[1,0]
	v_max_f32_e32 v120, 0, v120
	v_pk_mul_f32 v[126:127], v[126:127], v[156:157] op_sel_hi:[1,0]
	v_mul_f32_e32 v147, v120, v120
	v_max_f32_e32 v120, 0, v125
	v_max_f32_e32 v121, 0, v121
	v_max_f32_e32 v122, 0, v122
	v_max_f32_e32 v124, 0, v124
	v_mul_f32_e32 v120, v120, v120
	v_mul_f32_e32 v125, v121, v121
	v_max_f32_e32 v121, 0, v126
	v_mul_f32_e32 v126, v122, v122
	v_max_f32_e32 v122, 0, v127
	v_max_f32_e32 v123, 0, v123
	v_pk_mul_f32 v[114:115], v[114:115], v[156:157] op_sel_hi:[1,0]
	v_pk_mul_f32 v[112:113], v[112:113], v[156:157] op_sel_hi:[1,0]
	v_mul_f32_e32 v124, v124, v124
	v_mul_f32_e32 v121, v121, v121
	v_mul_f32_e32 v122, v122, v122
	v_mul_f32_e32 v123, v123, v123
	v_cvt_pk_bf16_f32 v120, v124, v120
	v_pk_mul_f32 v[118:119], v[118:119], v[156:157] op_sel_hi:[1,0]
	v_pk_mul_f32 v[116:117], v[116:117], v[156:157] op_sel_hi:[1,0]
	v_max_f32_e32 v112, 0, v112
	v_max_f32_e32 v113, 0, v113
	v_max_f32_e32 v114, 0, v114
	v_cvt_pk_bf16_f32 v121, v121, v122
	v_cvt_pk_bf16_f32 v122, v147, v125
	v_cvt_pk_bf16_f32 v123, v126, v123
	global_store_dwordx4 v[142:143], v[120:123], off
	v_max_f32_e32 v116, 0, v116
	v_max_f32_e32 v115, 0, v115
	v_mul_f32_e32 v120, v112, v112
	v_max_f32_e32 v112, 0, v117
	v_mul_f32_e32 v117, v113, v113
	v_max_f32_e32 v113, 0, v118
	v_mul_f32_e32 v118, v114, v114
	v_max_f32_e32 v114, 0, v119
	v_mul_f32_e32 v116, v116, v116
	v_mul_f32_e32 v112, v112, v112
	v_mul_f32_e32 v113, v113, v113
	v_mul_f32_e32 v114, v114, v114
	v_mul_f32_e32 v115, v115, v115
	v_cvt_pk_bf16_f32 v112, v116, v112
	v_cvt_pk_bf16_f32 v113, v113, v114
	v_cvt_pk_bf16_f32 v114, v120, v117
	v_cvt_pk_bf16_f32 v115, v118, v115
	ds_read_b128 v[116:119], v154 offset:256
	global_store_dwordx4 v[142:143], v[112:115], off offset:256
	s_nop 1
	v_or_b32_e32 v112, 16, v146
	s_waitcnt lgkmcnt(0)
	v_mov_b32_e32 v114, v117
	v_mov_b32_e32 v115, v118
	v_mov_b32_e32 v117, v119
	v_pk_add_f32 v[114:115], v[114:115], v[116:117]
	s_nop 0
	v_add_f32_e32 v113, v114, v115
	v_fmamk_f32 v113, v113, 0x3a800000, v198
	s_nop 1
	v_rsq_f32_e32 v114, v113
	v_ashrrev_i32_e32 v113, 31, v112
	v_lshlrev_b64 v[112:113], 13, v[112:113]
	v_lshl_add_u64 v[112:113], v[144:145], 0, v[112:113]
	v_pk_mul_f32 v[104:105], v[104:105], v[114:115] op_sel_hi:[1,0]
	v_pk_mul_f32 v[108:109], v[108:109], v[114:115] op_sel_hi:[1,0]
	v_pk_mul_f32 v[106:107], v[106:107], v[114:115] op_sel_hi:[1,0]
	v_max_f32_e32 v104, 0, v104
	v_pk_mul_f32 v[110:111], v[110:111], v[114:115] op_sel_hi:[1,0]
	v_mul_f32_e32 v115, v104, v104
	v_max_f32_e32 v104, 0, v109
	v_max_f32_e32 v105, 0, v105
	v_max_f32_e32 v106, 0, v106
	v_max_f32_e32 v108, 0, v108
	v_mul_f32_e32 v104, v104, v104
	v_mul_f32_e32 v109, v105, v105
	v_max_f32_e32 v105, 0, v110
	v_mul_f32_e32 v110, v106, v106
	v_max_f32_e32 v106, 0, v111
	v_max_f32_e32 v107, 0, v107
	v_pk_mul_f32 v[98:99], v[98:99], v[114:115] op_sel_hi:[1,0]
	v_pk_mul_f32 v[96:97], v[96:97], v[114:115] op_sel_hi:[1,0]
	v_mul_f32_e32 v108, v108, v108
	v_mul_f32_e32 v105, v105, v105
	v_mul_f32_e32 v106, v106, v106
	v_mul_f32_e32 v107, v107, v107
	v_cvt_pk_bf16_f32 v104, v108, v104
	v_pk_mul_f32 v[102:103], v[102:103], v[114:115] op_sel_hi:[1,0]
	v_pk_mul_f32 v[100:101], v[100:101], v[114:115] op_sel_hi:[1,0]
	v_max_f32_e32 v96, 0, v96
	v_max_f32_e32 v97, 0, v97
	v_max_f32_e32 v98, 0, v98
	v_cvt_pk_bf16_f32 v105, v105, v106
	v_cvt_pk_bf16_f32 v106, v115, v109
	v_cvt_pk_bf16_f32 v107, v110, v107
	global_store_dwordx4 v[112:113], v[104:107], off
	v_max_f32_e32 v100, 0, v100
	v_max_f32_e32 v99, 0, v99
	v_mul_f32_e32 v104, v96, v96
	v_max_f32_e32 v96, 0, v101
	v_mul_f32_e32 v101, v97, v97
	v_max_f32_e32 v97, 0, v102
	v_mul_f32_e32 v102, v98, v98
	v_max_f32_e32 v98, 0, v103
	v_mul_f32_e32 v100, v100, v100
	v_mul_f32_e32 v96, v96, v96
	v_mul_f32_e32 v97, v97, v97
	v_mul_f32_e32 v98, v98, v98
	v_mul_f32_e32 v99, v99, v99
	v_cvt_pk_bf16_f32 v96, v100, v96
	v_cvt_pk_bf16_f32 v97, v97, v98
	v_cvt_pk_bf16_f32 v98, v104, v101
	v_cvt_pk_bf16_f32 v99, v102, v99
	ds_read_b128 v[100:103], v154 offset:512
	global_store_dwordx4 v[112:113], v[96:99], off offset:256
	s_nop 1
	v_or_b32_e32 v96, 32, v146
	s_waitcnt lgkmcnt(0)
	v_mov_b32_e32 v98, v101
	v_mov_b32_e32 v99, v102
	v_mov_b32_e32 v101, v103
	v_pk_add_f32 v[98:99], v[98:99], v[100:101]
	s_nop 0
	v_add_f32_e32 v97, v98, v99
	v_fmamk_f32 v97, v97, 0x3a800000, v198
	s_nop 1
	v_rsq_f32_e32 v98, v97
	v_ashrrev_i32_e32 v97, 31, v96
	v_lshlrev_b64 v[96:97], 13, v[96:97]
	v_lshl_add_u64 v[96:97], v[144:145], 0, v[96:97]
	v_pk_mul_f32 v[88:89], v[88:89], v[98:99] op_sel_hi:[1,0]
	v_pk_mul_f32 v[92:93], v[92:93], v[98:99] op_sel_hi:[1,0]
	v_pk_mul_f32 v[90:91], v[90:91], v[98:99] op_sel_hi:[1,0]
	v_max_f32_e32 v88, 0, v88
	v_pk_mul_f32 v[94:95], v[94:95], v[98:99] op_sel_hi:[1,0]
	v_mul_f32_e32 v99, v88, v88
	v_max_f32_e32 v88, 0, v93
	v_max_f32_e32 v89, 0, v89
	v_max_f32_e32 v90, 0, v90
	v_max_f32_e32 v92, 0, v92
	v_mul_f32_e32 v88, v88, v88
	v_mul_f32_e32 v93, v89, v89
	v_max_f32_e32 v89, 0, v94
	v_mul_f32_e32 v94, v90, v90
	v_max_f32_e32 v90, 0, v95
	v_max_f32_e32 v91, 0, v91
	v_pk_mul_f32 v[82:83], v[82:83], v[98:99] op_sel_hi:[1,0]
	v_pk_mul_f32 v[80:81], v[80:81], v[98:99] op_sel_hi:[1,0]
	v_mul_f32_e32 v92, v92, v92
	v_mul_f32_e32 v89, v89, v89
	v_mul_f32_e32 v90, v90, v90
	v_mul_f32_e32 v91, v91, v91
	v_cvt_pk_bf16_f32 v88, v92, v88
	v_pk_mul_f32 v[86:87], v[86:87], v[98:99] op_sel_hi:[1,0]
	v_pk_mul_f32 v[84:85], v[84:85], v[98:99] op_sel_hi:[1,0]
	v_max_f32_e32 v80, 0, v80
	v_max_f32_e32 v81, 0, v81
	v_max_f32_e32 v82, 0, v82
	v_cvt_pk_bf16_f32 v89, v89, v90
	v_cvt_pk_bf16_f32 v90, v99, v93
	v_cvt_pk_bf16_f32 v91, v94, v91
	global_store_dwordx4 v[96:97], v[88:91], off
	v_max_f32_e32 v84, 0, v84
	v_max_f32_e32 v83, 0, v83
	v_mul_f32_e32 v88, v80, v80
	v_max_f32_e32 v80, 0, v85
	v_mul_f32_e32 v85, v81, v81
	v_max_f32_e32 v81, 0, v86
	v_mul_f32_e32 v86, v82, v82
	v_max_f32_e32 v82, 0, v87
	v_mul_f32_e32 v84, v84, v84
	v_mul_f32_e32 v80, v80, v80
	v_mul_f32_e32 v81, v81, v81
	v_mul_f32_e32 v82, v82, v82
	v_mul_f32_e32 v83, v83, v83
	v_cvt_pk_bf16_f32 v80, v84, v80
	v_cvt_pk_bf16_f32 v81, v81, v82
	v_cvt_pk_bf16_f32 v82, v88, v85
	v_cvt_pk_bf16_f32 v83, v86, v83
	ds_read_b128 v[84:87], v154 offset:768
	global_store_dwordx4 v[96:97], v[80:83], off offset:256
	s_nop 1
	v_or_b32_e32 v80, 48, v146
	s_waitcnt lgkmcnt(0)
	v_mov_b32_e32 v82, v85
	v_mov_b32_e32 v83, v86
	v_mov_b32_e32 v85, v87
	v_pk_add_f32 v[82:83], v[82:83], v[84:85]
	s_nop 0
	v_add_f32_e32 v81, v82, v83
	v_fmamk_f32 v81, v81, 0x3a800000, v198
	s_nop 1
	v_rsq_f32_e32 v82, v81
	v_ashrrev_i32_e32 v81, 31, v80
	v_lshlrev_b64 v[80:81], 13, v[80:81]
	v_lshl_add_u64 v[80:81], v[144:145], 0, v[80:81]
	v_pk_mul_f32 v[72:73], v[72:73], v[82:83] op_sel_hi:[1,0]
	v_pk_mul_f32 v[76:77], v[76:77], v[82:83] op_sel_hi:[1,0]
	v_pk_mul_f32 v[74:75], v[74:75], v[82:83] op_sel_hi:[1,0]
	v_max_f32_e32 v72, 0, v72
	v_pk_mul_f32 v[78:79], v[78:79], v[82:83] op_sel_hi:[1,0]
	v_mul_f32_e32 v83, v72, v72
	v_max_f32_e32 v72, 0, v77
	v_max_f32_e32 v73, 0, v73
	v_max_f32_e32 v74, 0, v74
	v_max_f32_e32 v76, 0, v76
	v_mul_f32_e32 v72, v72, v72
	v_mul_f32_e32 v77, v73, v73
	v_max_f32_e32 v73, 0, v78
	v_mul_f32_e32 v78, v74, v74
	v_max_f32_e32 v74, 0, v79
	v_max_f32_e32 v75, 0, v75
	v_pk_mul_f32 v[66:67], v[66:67], v[82:83] op_sel_hi:[1,0]
	v_pk_mul_f32 v[64:65], v[64:65], v[82:83] op_sel_hi:[1,0]
	v_mul_f32_e32 v76, v76, v76
	v_mul_f32_e32 v73, v73, v73
	v_mul_f32_e32 v74, v74, v74
	v_mul_f32_e32 v75, v75, v75
	v_cvt_pk_bf16_f32 v72, v76, v72
	v_pk_mul_f32 v[70:71], v[70:71], v[82:83] op_sel_hi:[1,0]
	v_pk_mul_f32 v[68:69], v[68:69], v[82:83] op_sel_hi:[1,0]
	v_max_f32_e32 v64, 0, v64
	v_max_f32_e32 v65, 0, v65
	v_max_f32_e32 v66, 0, v66
	v_cvt_pk_bf16_f32 v73, v73, v74
	v_cvt_pk_bf16_f32 v74, v83, v77
	v_cvt_pk_bf16_f32 v75, v78, v75
	global_store_dwordx4 v[80:81], v[72:75], off
	v_max_f32_e32 v68, 0, v68
	v_max_f32_e32 v67, 0, v67
	v_mul_f32_e32 v72, v64, v64
	v_max_f32_e32 v64, 0, v69
	v_mul_f32_e32 v69, v65, v65
	v_max_f32_e32 v65, 0, v70
	v_mul_f32_e32 v70, v66, v66
	v_max_f32_e32 v66, 0, v71
	v_mul_f32_e32 v68, v68, v68
	v_mul_f32_e32 v64, v64, v64
	v_mul_f32_e32 v65, v65, v65
	v_mul_f32_e32 v66, v66, v66
	v_mul_f32_e32 v67, v67, v67
	v_cvt_pk_bf16_f32 v64, v68, v64
	v_cvt_pk_bf16_f32 v65, v65, v66
	v_cvt_pk_bf16_f32 v66, v72, v69
	v_cvt_pk_bf16_f32 v67, v70, v67
	ds_read_b128 v[68:71], v154 offset:2048
	global_store_dwordx4 v[80:81], v[64:67], off offset:256
	s_waitcnt lgkmcnt(0)
	v_mov_b32_e32 v72, v69
	v_mov_b32_e32 v73, v70
	v_mov_b32_e32 v69, v71
	v_pk_add_f32 v[68:69], v[72:73], v[68:69]
	s_nop 0
	v_add_f32_e32 v68, v68, v69
	v_fmamk_f32 v68, v68, 0x3a800000, v198
	s_nop 1
	v_rsq_f32_e32 v68, v68
	s_nop 0
	v_mov_b32_e32 v64, v68
	v_pk_mul_f32 v[56:57], v[56:57], v[64:65] op_sel_hi:[1,0]
	v_pk_mul_f32 v[60:61], v[60:61], v[64:65] op_sel_hi:[1,0]
	v_pk_mul_f32 v[58:59], v[58:59], v[64:65] op_sel_hi:[1,0]
	v_max_f32_e32 v56, 0, v56
	v_pk_mul_f32 v[62:63], v[62:63], v[64:65] op_sel_hi:[1,0]
	v_max_f32_e32 v60, 0, v60
	v_mul_f32_e32 v65, v56, v56
	v_max_f32_e32 v56, 0, v61
	v_max_f32_e32 v57, 0, v57
	v_max_f32_e32 v58, 0, v58
	v_mul_f32_e32 v60, v60, v60
	v_mul_f32_e32 v56, v56, v56
	v_mul_f32_e32 v61, v57, v57
	v_max_f32_e32 v57, 0, v62
	v_mul_f32_e32 v62, v58, v58
	v_max_f32_e32 v58, 0, v63
	v_mul_f32_e32 v57, v57, v57
	v_max_f32_e32 v59, 0, v59
	v_mul_f32_e32 v58, v58, v58
	v_cvt_pk_bf16_f32 v56, v60, v56
	v_add_co_u32_e32 v60, vcc, s8, v142
	v_pk_mul_f32 v[50:51], v[50:51], v[64:65] op_sel_hi:[1,0]
	v_pk_mul_f32 v[48:49], v[48:49], v[64:65] op_sel_hi:[1,0]
	v_mul_f32_e32 v59, v59, v59
	v_cvt_pk_bf16_f32 v57, v57, v58
	v_cvt_pk_bf16_f32 v58, v65, v61
	v_addc_co_u32_e32 v61, vcc, 0, v143, vcc
	v_pk_mul_f32 v[54:55], v[54:55], v[64:65] op_sel_hi:[1,0]
	v_pk_mul_f32 v[52:53], v[52:53], v[64:65] op_sel_hi:[1,0]
	v_max_f32_e32 v48, 0, v48
	v_max_f32_e32 v49, 0, v49
	v_max_f32_e32 v50, 0, v50
	v_cvt_pk_bf16_f32 v59, v62, v59
	global_store_dwordx4 v[60:61], v[56:59], off
	v_max_f32_e32 v52, 0, v52
	v_max_f32_e32 v51, 0, v51
	v_mul_f32_e32 v56, v48, v48
	v_max_f32_e32 v48, 0, v53
	v_mul_f32_e32 v53, v49, v49
	v_max_f32_e32 v49, 0, v54
	v_mul_f32_e32 v54, v50, v50
	v_max_f32_e32 v50, 0, v55
	v_mul_f32_e32 v52, v52, v52
	v_mul_f32_e32 v48, v48, v48
	v_mul_f32_e32 v49, v49, v49
	v_mul_f32_e32 v50, v50, v50
	v_mul_f32_e32 v51, v51, v51
	v_cvt_pk_bf16_f32 v48, v52, v48
	v_cvt_pk_bf16_f32 v49, v49, v50
	v_cvt_pk_bf16_f32 v50, v56, v53
	v_cvt_pk_bf16_f32 v51, v54, v51
	ds_read_b128 v[52:55], v154 offset:2304
	s_mov_b64 s[8:9], 0x100000
	s_waitcnt lgkmcnt(0)
	v_mov_b32_e32 v56, v53
	v_mov_b32_e32 v57, v54
	v_mov_b32_e32 v53, v55
	v_pk_add_f32 v[52:53], v[56:57], v[52:53]
	s_nop 0
	v_add_f32_e32 v52, v52, v53
	v_fmamk_f32 v52, v52, 0x3a800000, v198
	s_nop 1
	v_rsq_f32_e32 v54, v52
	v_lshl_add_u64 v[52:53], v[142:143], 0, s[8:9]
	global_store_dwordx4 v[52:53], v[48:51], off offset:256
	s_mov_b32 s8, 0x120000
	s_nop 0
	v_mov_b32_e32 v48, v54
	v_pk_mul_f32 v[40:41], v[40:41], v[48:49] op_sel_hi:[1,0]
	v_pk_mul_f32 v[44:45], v[44:45], v[48:49] op_sel_hi:[1,0]
	v_pk_mul_f32 v[42:43], v[42:43], v[48:49] op_sel_hi:[1,0]
	v_max_f32_e32 v40, 0, v40
	v_pk_mul_f32 v[46:47], v[46:47], v[48:49] op_sel_hi:[1,0]
	v_max_f32_e32 v44, 0, v44
	v_mul_f32_e32 v49, v40, v40
	v_max_f32_e32 v40, 0, v45
	v_max_f32_e32 v41, 0, v41
	v_max_f32_e32 v42, 0, v42
	v_mul_f32_e32 v44, v44, v44
	v_mul_f32_e32 v40, v40, v40
	v_mul_f32_e32 v45, v41, v41
	v_max_f32_e32 v41, 0, v46
	v_mul_f32_e32 v46, v42, v42
	v_max_f32_e32 v42, 0, v47
	v_mul_f32_e32 v41, v41, v41
	v_max_f32_e32 v43, 0, v43
	v_mul_f32_e32 v42, v42, v42
	v_cvt_pk_bf16_f32 v40, v44, v40
	v_add_co_u32_e32 v44, vcc, s8, v142
	v_pk_mul_f32 v[34:35], v[34:35], v[48:49] op_sel_hi:[1,0]
	v_pk_mul_f32 v[32:33], v[32:33], v[48:49] op_sel_hi:[1,0]
	v_mul_f32_e32 v43, v43, v43
	v_cvt_pk_bf16_f32 v41, v41, v42
	v_cvt_pk_bf16_f32 v42, v49, v45
	v_addc_co_u32_e32 v45, vcc, 0, v143, vcc
	v_pk_mul_f32 v[38:39], v[38:39], v[48:49] op_sel_hi:[1,0]
	v_pk_mul_f32 v[36:37], v[36:37], v[48:49] op_sel_hi:[1,0]
	v_max_f32_e32 v32, 0, v32
	v_max_f32_e32 v33, 0, v33
	v_max_f32_e32 v34, 0, v34
	v_cvt_pk_bf16_f32 v43, v46, v43
	global_store_dwordx4 v[44:45], v[40:43], off
	v_max_f32_e32 v36, 0, v36
	v_max_f32_e32 v35, 0, v35
	v_mul_f32_e32 v40, v32, v32
	v_max_f32_e32 v32, 0, v37
	v_mul_f32_e32 v37, v33, v33
	v_max_f32_e32 v33, 0, v38
	v_mul_f32_e32 v38, v34, v34
	v_max_f32_e32 v34, 0, v39
	v_mul_f32_e32 v36, v36, v36
	v_mul_f32_e32 v32, v32, v32
	v_mul_f32_e32 v33, v33, v33
	v_mul_f32_e32 v34, v34, v34
	v_mul_f32_e32 v35, v35, v35
	v_cvt_pk_bf16_f32 v32, v36, v32
	v_cvt_pk_bf16_f32 v33, v33, v34
	v_cvt_pk_bf16_f32 v34, v40, v37
	v_cvt_pk_bf16_f32 v35, v38, v35
	ds_read_b128 v[36:39], v154 offset:2560
	s_mov_b64 s[8:9], 0x120000
	s_waitcnt lgkmcnt(0)
	v_mov_b32_e32 v40, v37
	v_mov_b32_e32 v41, v38
	v_mov_b32_e32 v37, v39
	v_pk_add_f32 v[36:37], v[40:41], v[36:37]
	s_nop 0
	v_add_f32_e32 v36, v36, v37
	v_fmamk_f32 v36, v36, 0x3a800000, v198
	s_nop 1
	v_rsq_f32_e32 v38, v36
	v_lshl_add_u64 v[36:37], v[142:143], 0, s[8:9]
	global_store_dwordx4 v[36:37], v[32:35], off offset:256
	s_mov_b32 s8, 0x140000
	s_nop 0
	v_mov_b32_e32 v32, v38
	v_pk_mul_f32 v[24:25], v[24:25], v[32:33] op_sel_hi:[1,0]
	v_pk_mul_f32 v[28:29], v[28:29], v[32:33] op_sel_hi:[1,0]
	v_pk_mul_f32 v[26:27], v[26:27], v[32:33] op_sel_hi:[1,0]
	v_max_f32_e32 v24, 0, v24
	v_pk_mul_f32 v[30:31], v[30:31], v[32:33] op_sel_hi:[1,0]
	v_max_f32_e32 v28, 0, v28
	v_mul_f32_e32 v33, v24, v24
	v_max_f32_e32 v24, 0, v29
	v_max_f32_e32 v25, 0, v25
	v_max_f32_e32 v26, 0, v26
	v_mul_f32_e32 v28, v28, v28
	v_mul_f32_e32 v24, v24, v24
	v_mul_f32_e32 v29, v25, v25
	v_max_f32_e32 v25, 0, v30
	v_mul_f32_e32 v30, v26, v26
	v_max_f32_e32 v26, 0, v31
	v_mul_f32_e32 v25, v25, v25
	v_max_f32_e32 v27, 0, v27
	v_mul_f32_e32 v26, v26, v26
	v_cvt_pk_bf16_f32 v24, v28, v24
	v_add_co_u32_e32 v28, vcc, s8, v142
	v_pk_mul_f32 v[18:19], v[18:19], v[32:33] op_sel_hi:[1,0]
	v_pk_mul_f32 v[16:17], v[16:17], v[32:33] op_sel_hi:[1,0]
	v_mul_f32_e32 v27, v27, v27
	v_cvt_pk_bf16_f32 v25, v25, v26
	v_cvt_pk_bf16_f32 v26, v33, v29
	v_addc_co_u32_e32 v29, vcc, 0, v143, vcc
	v_pk_mul_f32 v[22:23], v[22:23], v[32:33] op_sel_hi:[1,0]
	v_pk_mul_f32 v[20:21], v[20:21], v[32:33] op_sel_hi:[1,0]
	v_max_f32_e32 v16, 0, v16
	v_max_f32_e32 v17, 0, v17
	v_max_f32_e32 v18, 0, v18
	v_cvt_pk_bf16_f32 v27, v30, v27
	global_store_dwordx4 v[28:29], v[24:27], off
	v_max_f32_e32 v20, 0, v20
	v_max_f32_e32 v19, 0, v19
	v_mul_f32_e32 v24, v16, v16
	v_max_f32_e32 v16, 0, v21
	v_mul_f32_e32 v21, v17, v17
	v_max_f32_e32 v17, 0, v22
	v_mul_f32_e32 v22, v18, v18
	v_max_f32_e32 v18, 0, v23
	v_mul_f32_e32 v20, v20, v20
	v_mul_f32_e32 v16, v16, v16
	v_mul_f32_e32 v17, v17, v17
	v_mul_f32_e32 v18, v18, v18
	v_mul_f32_e32 v19, v19, v19
	v_cvt_pk_bf16_f32 v16, v20, v16
	v_cvt_pk_bf16_f32 v17, v17, v18
	v_cvt_pk_bf16_f32 v18, v24, v21
	v_cvt_pk_bf16_f32 v19, v22, v19
	ds_read_b128 v[20:23], v154 offset:2816
	s_mov_b64 s[8:9], 0x140000
	s_waitcnt lgkmcnt(0)
	v_mov_b32_e32 v24, v21
	v_mov_b32_e32 v25, v22
	v_mov_b32_e32 v21, v23
	v_pk_add_f32 v[20:21], v[24:25], v[20:21]
	s_nop 0
	v_add_f32_e32 v20, v20, v21
	v_fmamk_f32 v20, v20, 0x3a800000, v198
	s_nop 1
	v_rsq_f32_e32 v22, v20
	v_lshl_add_u64 v[20:21], v[142:143], 0, s[8:9]
	global_store_dwordx4 v[20:21], v[16:19], off offset:256
	s_mov_b64 s[8:9], 0x160000
	s_nop 0
	v_mov_b32_e32 v18, v22
	v_pk_mul_f32 v[8:9], v[8:9], v[18:19] op_sel_hi:[1,0]
	v_pk_mul_f32 v[12:13], v[12:13], v[18:19] op_sel_hi:[1,0]
	v_pk_mul_f32 v[10:11], v[10:11], v[18:19] op_sel_hi:[1,0]
	v_max_f32_e32 v8, 0, v8
	v_pk_mul_f32 v[14:15], v[14:15], v[18:19] op_sel_hi:[1,0]
	v_max_f32_e32 v12, 0, v12
	v_mul_f32_e32 v19, v8, v8
	v_max_f32_e32 v8, 0, v13
	v_max_f32_e32 v9, 0, v9
	v_max_f32_e32 v10, 0, v10
	v_lshl_add_u64 v[16:17], v[142:143], 0, s[8:9]
	v_mul_f32_e32 v12, v12, v12
	v_mul_f32_e32 v8, v8, v8
	v_mul_f32_e32 v13, v9, v9
	v_max_f32_e32 v9, 0, v14
	v_mul_f32_e32 v14, v10, v10
	v_max_f32_e32 v10, 0, v15
	s_mov_b32 s8, 0x160000
	v_mul_f32_e32 v9, v9, v9
	v_max_f32_e32 v11, 0, v11
	v_mul_f32_e32 v10, v10, v10
	v_cvt_pk_bf16_f32 v8, v12, v8
	v_add_co_u32_e32 v12, vcc, s8, v142
	v_pk_mul_f32 v[2:3], v[2:3], v[18:19] op_sel_hi:[1,0]
	v_pk_mul_f32 v[0:1], v[0:1], v[18:19] op_sel_hi:[1,0]
	v_mul_f32_e32 v11, v11, v11
	v_cvt_pk_bf16_f32 v9, v9, v10
	v_cvt_pk_bf16_f32 v10, v19, v13
	v_addc_co_u32_e32 v13, vcc, 0, v143, vcc
	v_pk_mul_f32 v[6:7], v[6:7], v[18:19] op_sel_hi:[1,0]
	v_pk_mul_f32 v[4:5], v[4:5], v[18:19] op_sel_hi:[1,0]
	v_max_f32_e32 v0, 0, v0
	v_max_f32_e32 v1, 0, v1
	v_max_f32_e32 v2, 0, v2
	v_cvt_pk_bf16_f32 v11, v14, v11
	global_store_dwordx4 v[12:13], v[8:11], off
	v_max_f32_e32 v3, 0, v3
	v_max_f32_e32 v4, 0, v4
	v_mul_f32_e32 v8, v0, v0
	v_max_f32_e32 v0, 0, v5
	v_mul_f32_e32 v5, v1, v1
	v_max_f32_e32 v1, 0, v6
	v_mul_f32_e32 v6, v2, v2
	v_max_f32_e32 v2, 0, v7
	v_mul_f32_e32 v0, v0, v0
	v_mul_f32_e32 v1, v1, v1
	v_mul_f32_e32 v2, v2, v2
	v_mul_f32_e32 v3, v3, v3
	s_andn2_b64 vcc, exec, s[42:43]
	s_mov_b64 s[42:43], -1
	v_mul_f32_e32 v4, v4, v4
	v_cvt_pk_bf16_f32 v0, v4, v0
	v_cvt_pk_bf16_f32 v1, v1, v2
	v_cvt_pk_bf16_f32 v2, v8, v5
	v_cvt_pk_bf16_f32 v3, v6, v3
	global_store_dwordx4 v[16:17], v[0:3], off offset:256
	s_cbranch_vccnz .LBB0_1677
	s_andn2_b64 vcc, exec, s[26:27]
	s_cbranch_vccnz .LBB0_1676
	s_barrier
	s_branch .LBB0_1676
